# speedup vs baseline: 1.0099x; 1.0040x over previous
.Lrs_a_4:
	s_add_u32 s81, s40, s22
	s_addc_u32 s82, s41, s23
	s_add_u32 s29, s40, 0x100
	s_addc_u32 s44, s41, 0
	s_and_b64 s[42:43], s[14:15], exec
	ds_read_b128 v[82:85], v161
	ds_read_b128 v[94:97], v161 offset:2048
	ds_read_b128 v[102:105], v162
	ds_read_b128 v[110:113], v162 offset:2048
	s_cselect_b32 s47, s37, s44
	s_cselect_b32 s46, s36, s29
	s_add_u32 s29, s38, 0x100
	s_addc_u32 s44, s39, 0
	s_and_b64 s[42:43], s[14:15], exec
	s_cselect_b32 s49, s5, s44
	s_cselect_b32 s48, s4, s29
	s_add_u32 s44, s46, 0x80
	s_addc_u32 s45, s47, 0
	s_add_u32 s42, s48, 0x80
	s_addc_u32 s43, s49, 0
	ds_read_b128 v[58:61], v163
	ds_read_b128 v[66:69], v163 offset:2048
	ds_read_b128 v[62:65], v164
	ds_read_b128 v[70:73], v164 offset:2048
	ds_read_b128 v[74:77], v163 offset:4096
	ds_read_b128 v[86:89], v163 offset:6144
	ds_read_b128 v[78:81], v164 offset:4096
	ds_read_b128 v[90:93], v164 offset:6144
	s_add_u32 s78, s81, 0x80
	s_addc_u32 s79, s82, 0
	s_mov_b32 m0, s70
	s_nop 0
	global_load_lds_dwordx4 v146, s[78:79]
	s_mov_b32 m0, s71
	s_nop 0
	global_load_lds_dwordx4 v150, s[78:79]
	s_waitcnt lgkmcnt(8)
	ds_read_b128 v[142:145], v161 offset:16384
	ds_read_b128 v[166:169], v161 offset:18432
	ds_read_b128 v[170:173], v162 offset:16384
	ds_read_b128 v[174:177], v162 offset:18432
	s_waitcnt vmcnt(8)
	s_waitcnt lgkmcnt(0)
	s_barrier
	s_waitcnt lgkmcnt(0)
	s_waitcnt vmcnt(16)
	v_mov_b32_e32 v1, v0
	v_pk_mul_f32 v[16:17], v[0:1], v[16:17]
	v_pk_mul_f32 v[14:15], v[154:155], v[14:15]
	v_pk_mul_f32 v[12:13], v[0:1], v[12:13]
	v_pk_mul_f32 v[10:11], v[154:155], v[10:11]
	v_pk_mul_f32 v[8:9], v[0:1], v[8:9]
	v_pk_mul_f32 v[6:7], v[154:155], v[6:7]
	v_pk_mul_f32 v[4:5], v[0:1], v[4:5]
	v_pk_mul_f32 v[2:3], v[154:155], v[2:3]
	s_setprio 1
	v_mfma_f32_16x16x128_f8f6f4 v[18:21], v[82:85], v[58:61], v[14:17] cbsz:4 blgp:4
	v_mfma_f32_16x16x128_f8f6f4 v[18:21], v[102:105], v[62:65], v[18:21] cbsz:4 blgp:4
	v_mfma_f32_16x16x128_f8f6f4 v[26:29], v[82:85], v[66:69], v[14:17] cbsz:4 blgp:4
	v_mfma_f32_16x16x128_f8f6f4 v[26:29], v[102:105], v[70:73], v[26:29] cbsz:4 blgp:4
	v_mfma_f32_16x16x128_f8f6f4 v[34:37], v[82:85], v[74:77], v[14:17] cbsz:4 blgp:4
	v_mfma_f32_16x16x128_f8f6f4 v[34:37], v[102:105], v[78:81], v[34:37] cbsz:4 blgp:4
	v_mfma_f32_16x16x128_f8f6f4 v[42:45], v[82:85], v[86:89], v[14:17] cbsz:4 blgp:4
	v_mfma_f32_16x16x128_f8f6f4 v[42:45], v[102:105], v[90:93], v[42:45] cbsz:4 blgp:4
	v_mfma_f32_16x16x128_f8f6f4 v[22:25], v[94:97], v[58:61], v[10:13] cbsz:4 blgp:4
	v_mfma_f32_16x16x128_f8f6f4 v[22:25], v[110:113], v[62:65], v[22:25] cbsz:4 blgp:4
	v_mfma_f32_16x16x128_f8f6f4 v[30:33], v[94:97], v[66:69], v[10:13] cbsz:4 blgp:4
	v_mfma_f32_16x16x128_f8f6f4 v[30:33], v[110:113], v[70:73], v[30:33] cbsz:4 blgp:4
	v_mfma_f32_16x16x128_f8f6f4 v[38:41], v[94:97], v[74:77], v[10:13] cbsz:4 blgp:4
	v_mfma_f32_16x16x128_f8f6f4 v[38:41], v[110:113], v[78:81], v[38:41] cbsz:4 blgp:4
	v_mfma_f32_16x16x128_f8f6f4 v[46:49], v[94:97], v[86:89], v[10:13] cbsz:4 blgp:4
	v_mfma_f32_16x16x128_f8f6f4 v[46:49], v[110:113], v[90:93], v[46:49] cbsz:4 blgp:4
	v_mfma_f32_16x16x128_f8f6f4 v[50:53], v[142:145], v[58:61], v[6:9] cbsz:4 blgp:4
	v_mfma_f32_16x16x128_f8f6f4 v[50:53], v[170:173], v[62:65], v[50:53] cbsz:4 blgp:4
	v_mfma_f32_16x16x128_f8f6f4 v[54:57], v[166:169], v[58:61], v[2:5] cbsz:4 blgp:4
	v_mfma_f32_16x16x128_f8f6f4 v[54:57], v[174:177], v[62:65], v[54:57] cbsz:4 blgp:4
	v_mfma_f32_16x16x128_f8f6f4 v[58:61], v[142:145], v[66:69], v[6:9] cbsz:4 blgp:4
	v_mfma_f32_16x16x128_f8f6f4 v[58:61], v[170:173], v[70:73], v[58:61] cbsz:4 blgp:4
	v_mfma_f32_16x16x128_f8f6f4 v[62:65], v[166:169], v[66:69], v[2:5] cbsz:4 blgp:4
	v_mfma_f32_16x16x128_f8f6f4 v[62:65], v[174:177], v[70:73], v[62:65] cbsz:4 blgp:4
	v_mfma_f32_16x16x128_f8f6f4 v[66:69], v[142:145], v[74:77], v[6:9] cbsz:4 blgp:4
	v_mfma_f32_16x16x128_f8f6f4 v[66:69], v[170:173], v[78:81], v[66:69] cbsz:4 blgp:4
	v_mfma_f32_16x16x128_f8f6f4 v[70:73], v[166:169], v[74:77], v[2:5] cbsz:4 blgp:4
	v_mfma_f32_16x16x128_f8f6f4 v[70:73], v[174:177], v[78:81], v[70:73] cbsz:4 blgp:4
	v_mfma_f32_16x16x128_f8f6f4 v[74:77], v[142:145], v[86:89], v[6:9] cbsz:4 blgp:4
	v_mfma_f32_16x16x128_f8f6f4 v[74:77], v[170:173], v[90:93], v[74:77] cbsz:4 blgp:4
	v_mfma_f32_16x16x128_f8f6f4 v[78:81], v[166:169], v[86:89], v[2:5] cbsz:4 blgp:4
	v_mfma_f32_16x16x128_f8f6f4 v[78:81], v[174:177], v[90:93], v[78:81] cbsz:4 blgp:4
	s_setprio 0
	s_barrier
	s_mov_b32 m0, s55
	s_nop 0
	global_load_lds_dwordx4 v148, s[48:49]
	s_mov_b32 m0, s56
	s_nop 0
	global_load_lds_dwordx4 v152, s[48:49]
	ds_read_b128 v[114:117], v163 offset:16384
	ds_read_b128 v[122:125], v163 offset:18432
	ds_read_b128 v[130:133], v164 offset:16384
	ds_read_b128 v[134:137], v164 offset:18432
	ds_read_b128 v[178:181], v163 offset:20480
	ds_read_b128 v[182:185], v163 offset:22528
	ds_read_b128 v[186:189], v164 offset:20480
	ds_read_b128 v[190:193], v164 offset:22528
	s_mov_b32 m0, s54
	s_nop 0
	global_load_lds_dwordx4 v146, s[46:47]
	s_mov_b32 m0, s57
	s_nop 0
	global_load_lds_dwordx4 v150, s[46:47]
	s_add_u32 s48, s48, s24
	s_addc_u32 s49, s49, s25
	s_mov_b32 m0, s58
	s_nop 0
	global_load_lds_dwordx4 v148, s[48:49]
	s_mov_b32 m0, s59
	s_nop 0
	global_load_lds_dwordx4 v152, s[48:49]
	s_waitcnt vmcnt(8)
	s_waitcnt lgkmcnt(0)
	s_barrier
	s_setprio 1
	v_mfma_f32_16x16x128_f8f6f4 v[86:89], v[82:85], v[114:117], v[14:17] cbsz:4 blgp:4
	v_mfma_f32_16x16x128_f8f6f4 v[86:89], v[102:105], v[130:133], v[86:89] cbsz:4 blgp:4
	v_mfma_f32_16x16x128_f8f6f4 v[98:101], v[82:85], v[122:125], v[14:17] cbsz:4 blgp:4
	v_mfma_f32_16x16x128_f8f6f4 v[98:101], v[102:105], v[134:137], v[98:101] cbsz:4 blgp:4
	v_mfma_f32_16x16x128_f8f6f4 v[118:121], v[82:85], v[178:181], v[14:17] cbsz:4 blgp:4
	v_mfma_f32_16x16x128_f8f6f4 v[118:121], v[102:105], v[186:189], v[118:121] cbsz:4 blgp:4
	v_mfma_f32_16x16x128_f8f6f4 v[138:141], v[82:85], v[182:185], v[14:17] cbsz:4 blgp:4
	v_mfma_f32_16x16x128_f8f6f4 v[138:141], v[102:105], v[190:193], v[138:141] cbsz:4 blgp:4
	v_mfma_f32_16x16x128_f8f6f4 v[90:93], v[94:97], v[114:117], v[10:13] cbsz:4 blgp:4
	v_mfma_f32_16x16x128_f8f6f4 v[90:93], v[110:113], v[130:133], v[90:93] cbsz:4 blgp:4
	v_mfma_f32_16x16x128_f8f6f4 v[106:109], v[94:97], v[122:125], v[10:13] cbsz:4 blgp:4
	v_mfma_f32_16x16x128_f8f6f4 v[106:109], v[110:113], v[134:137], v[106:109] cbsz:4 blgp:4
	v_mfma_f32_16x16x128_f8f6f4 v[126:129], v[94:97], v[178:181], v[10:13] cbsz:4 blgp:4
	v_mfma_f32_16x16x128_f8f6f4 v[126:129], v[110:113], v[186:189], v[126:129] cbsz:4 blgp:4
	v_mfma_f32_16x16x128_f8f6f4 v[82:85], v[94:97], v[182:185], v[10:13] cbsz:4 blgp:4
	v_mfma_f32_16x16x128_f8f6f4 v[82:85], v[110:113], v[190:193], v[82:85] cbsz:4 blgp:4
	v_mfma_f32_16x16x128_f8f6f4 v[94:97], v[142:145], v[114:117], v[6:9] cbsz:4 blgp:4
	v_mfma_f32_16x16x128_f8f6f4 v[94:97], v[170:173], v[130:133], v[94:97] cbsz:4 blgp:4
	v_mfma_f32_16x16x128_f8f6f4 v[102:105], v[166:169], v[114:117], v[2:5] cbsz:4 blgp:4
	v_mfma_f32_16x16x128_f8f6f4 v[102:105], v[174:177], v[130:133], v[102:105] cbsz:4 blgp:4
	v_mfma_f32_16x16x128_f8f6f4 v[110:113], v[142:145], v[122:125], v[6:9] cbsz:4 blgp:4
	v_mfma_f32_16x16x128_f8f6f4 v[110:113], v[170:173], v[134:137], v[110:113] cbsz:4 blgp:4
	v_mfma_f32_16x16x128_f8f6f4 v[114:117], v[166:169], v[122:125], v[2:5] cbsz:4 blgp:4
	v_mfma_f32_16x16x128_f8f6f4 v[114:117], v[174:177], v[134:137], v[114:117] cbsz:4 blgp:4
	v_mfma_f32_16x16x128_f8f6f4 v[122:125], v[142:145], v[178:181], v[6:9] cbsz:4 blgp:4
	v_mfma_f32_16x16x128_f8f6f4 v[122:125], v[170:173], v[186:189], v[122:125] cbsz:4 blgp:4
	v_mfma_f32_16x16x128_f8f6f4 v[130:133], v[166:169], v[178:181], v[2:5] cbsz:4 blgp:4
	v_mfma_f32_16x16x128_f8f6f4 v[130:133], v[174:177], v[186:189], v[130:133] cbsz:4 blgp:4
	v_mfma_f32_16x16x128_f8f6f4 v[134:137], v[142:145], v[182:185], v[6:9] cbsz:4 blgp:4
	v_mfma_f32_16x16x128_f8f6f4 v[134:137], v[170:173], v[190:193], v[134:137] cbsz:4 blgp:4
	v_mfma_f32_16x16x128_f8f6f4 v[142:145], v[166:169], v[182:185], v[2:5] cbsz:4 blgp:4
	v_mfma_f32_16x16x128_f8f6f4 v[142:145], v[174:177], v[190:193], v[142:145] cbsz:4 blgp:4
	s_setprio 0
	s_barrier
	ds_read_b128 v[166:169], v161 offset:32768
	ds_read_b128 v[170:173], v161 offset:34816
	ds_read_b128 v[174:177], v162 offset:32768
	ds_read_b128 v[178:181], v162 offset:34816
	ds_read_b128 v[182:185], v163 offset:32768
	ds_read_b128 v[186:189], v163 offset:34816
	ds_read_b128 v[190:193], v164 offset:32768
	ds_read_b128 v[194:197], v164 offset:34816
	ds_read_b128 v[198:201], v163 offset:36864
	ds_read_b128 v[202:205], v163 offset:38912
	ds_read_b128 v[206:209], v164 offset:36864
	ds_read_b128 v[210:213], v164 offset:38912
	s_add_u32 s46, s46, s22
	s_addc_u32 s47, s47, s23
	s_mov_b32 m0, s60
	s_nop 0
	global_load_lds_dwordx4 v146, s[46:47]
	s_mov_b32 m0, s61
	s_nop 0
	global_load_lds_dwordx4 v150, s[46:47]
	s_waitcnt lgkmcnt(8)
	ds_read_b128 v[214:217], v161 offset:49152
	ds_read_b128 v[218:221], v161 offset:51200
	ds_read_b128 v[222:225], v162 offset:49152
	ds_read_b128 v[226:229], v162 offset:51200
	s_waitcnt vmcnt(8)
	s_waitcnt lgkmcnt(0)
	s_barrier
	s_waitcnt lgkmcnt(0)
	s_setprio 1
	v_mfma_f32_16x16x128_f8f6f4 v[18:21], v[166:169], v[182:185], v[18:21] cbsz:4 blgp:4
	v_mfma_f32_16x16x128_f8f6f4 v[18:21], v[174:177], v[190:193], v[18:21] cbsz:4 blgp:4
	v_mfma_f32_16x16x128_f8f6f4 v[26:29], v[166:169], v[186:189], v[26:29] cbsz:4 blgp:4
	v_mfma_f32_16x16x128_f8f6f4 v[26:29], v[174:177], v[194:197], v[26:29] cbsz:4 blgp:4
	v_mfma_f32_16x16x128_f8f6f4 v[34:37], v[166:169], v[198:201], v[34:37] cbsz:4 blgp:4
	v_mfma_f32_16x16x128_f8f6f4 v[34:37], v[174:177], v[206:209], v[34:37] cbsz:4 blgp:4
	v_mfma_f32_16x16x128_f8f6f4 v[42:45], v[166:169], v[202:205], v[42:45] cbsz:4 blgp:4
	v_mfma_f32_16x16x128_f8f6f4 v[42:45], v[174:177], v[210:213], v[42:45] cbsz:4 blgp:4
	v_mfma_f32_16x16x128_f8f6f4 v[22:25], v[170:173], v[182:185], v[22:25] cbsz:4 blgp:4
	v_mfma_f32_16x16x128_f8f6f4 v[22:25], v[178:181], v[190:193], v[22:25] cbsz:4 blgp:4
	v_mfma_f32_16x16x128_f8f6f4 v[30:33], v[170:173], v[186:189], v[30:33] cbsz:4 blgp:4
	v_mfma_f32_16x16x128_f8f6f4 v[30:33], v[178:181], v[194:197], v[30:33] cbsz:4 blgp:4
	v_mfma_f32_16x16x128_f8f6f4 v[38:41], v[170:173], v[198:201], v[38:41] cbsz:4 blgp:4
	v_mfma_f32_16x16x128_f8f6f4 v[38:41], v[178:181], v[206:209], v[38:41] cbsz:4 blgp:4
	v_mfma_f32_16x16x128_f8f6f4 v[46:49], v[170:173], v[202:205], v[46:49] cbsz:4 blgp:4
	v_mfma_f32_16x16x128_f8f6f4 v[46:49], v[178:181], v[210:213], v[46:49] cbsz:4 blgp:4
	v_mfma_f32_16x16x128_f8f6f4 v[50:53], v[214:217], v[182:185], v[50:53] cbsz:4 blgp:4
	v_mfma_f32_16x16x128_f8f6f4 v[50:53], v[222:225], v[190:193], v[50:53] cbsz:4 blgp:4
	v_mfma_f32_16x16x128_f8f6f4 v[58:61], v[214:217], v[186:189], v[58:61] cbsz:4 blgp:4
	v_mfma_f32_16x16x128_f8f6f4 v[58:61], v[222:225], v[194:197], v[58:61] cbsz:4 blgp:4
	v_mfma_f32_16x16x128_f8f6f4 v[66:69], v[214:217], v[198:201], v[66:69] cbsz:4 blgp:4
	v_mfma_f32_16x16x128_f8f6f4 v[66:69], v[222:225], v[206:209], v[66:69] cbsz:4 blgp:4
	v_mfma_f32_16x16x128_f8f6f4 v[74:77], v[214:217], v[202:205], v[74:77] cbsz:4 blgp:4
	v_mfma_f32_16x16x128_f8f6f4 v[74:77], v[222:225], v[210:213], v[74:77] cbsz:4 blgp:4
	v_mfma_f32_16x16x128_f8f6f4 v[54:57], v[218:221], v[182:185], v[54:57] cbsz:4 blgp:4
	v_mfma_f32_16x16x128_f8f6f4 v[54:57], v[226:229], v[190:193], v[54:57] cbsz:4 blgp:4
	v_mfma_f32_16x16x128_f8f6f4 v[62:65], v[218:221], v[186:189], v[62:65] cbsz:4 blgp:4
	v_mfma_f32_16x16x128_f8f6f4 v[62:65], v[226:229], v[194:197], v[62:65] cbsz:4 blgp:4
	v_mfma_f32_16x16x128_f8f6f4 v[70:73], v[218:221], v[198:201], v[70:73] cbsz:4 blgp:4
	v_mfma_f32_16x16x128_f8f6f4 v[70:73], v[226:229], v[206:209], v[70:73] cbsz:4 blgp:4
	v_mfma_f32_16x16x128_f8f6f4 v[78:81], v[218:221], v[202:205], v[78:81] cbsz:4 blgp:4
	v_mfma_f32_16x16x128_f8f6f4 v[78:81], v[226:229], v[210:213], v[78:81] cbsz:4 blgp:4
	s_setprio 0
	s_barrier
	s_mov_b32 m0, s64
	s_nop 0
	global_load_lds_dwordx4 v148, s[42:43]
	s_mov_b32 m0, s65
	s_nop 0
	global_load_lds_dwordx4 v152, s[42:43]
	ds_read_b128 v[182:185], v163 offset:49152
	ds_read_b128 v[186:189], v163 offset:51200
	ds_read_b128 v[190:193], v164 offset:49152
	ds_read_b128 v[194:197], v164 offset:51200
	ds_read_b128 v[198:201], v163 offset:53248
	ds_read_b128 v[202:205], v163 offset:55296
	ds_read_b128 v[206:209], v164 offset:53248
	ds_read_b128 v[210:213], v164 offset:55296
	s_mov_b32 m0, s66
	s_nop 0
	global_load_lds_dwordx4 v146, s[44:45]
	s_mov_b32 m0, s67
	s_nop 0
	global_load_lds_dwordx4 v150, s[44:45]
	s_add_u32 s42, s42, s24
	s_addc_u32 s43, s43, s25
	s_mov_b32 m0, s68
	s_nop 0
	global_load_lds_dwordx4 v148, s[42:43]
	s_mov_b32 m0, s69
	s_nop 0
	global_load_lds_dwordx4 v152, s[42:43]
	s_waitcnt vmcnt(8)
	s_waitcnt lgkmcnt(0)
	s_barrier
	s_setprio 1
	v_mfma_f32_16x16x128_f8f6f4 v[86:89], v[166:169], v[182:185], v[86:89] cbsz:4 blgp:4
	v_mfma_f32_16x16x128_f8f6f4 v[86:89], v[174:177], v[190:193], v[86:89] cbsz:4 blgp:4
	v_mfma_f32_16x16x128_f8f6f4 v[98:101], v[166:169], v[186:189], v[98:101] cbsz:4 blgp:4
	v_mfma_f32_16x16x128_f8f6f4 v[98:101], v[174:177], v[194:197], v[98:101] cbsz:4 blgp:4
	v_mfma_f32_16x16x128_f8f6f4 v[118:121], v[166:169], v[198:201], v[118:121] cbsz:4 blgp:4
	v_mfma_f32_16x16x128_f8f6f4 v[118:121], v[174:177], v[206:209], v[118:121] cbsz:4 blgp:4
	v_mfma_f32_16x16x128_f8f6f4 v[138:141], v[166:169], v[202:205], v[138:141] cbsz:4 blgp:4
	v_mfma_f32_16x16x128_f8f6f4 v[138:141], v[174:177], v[210:213], v[138:141] cbsz:4 blgp:4
	v_mfma_f32_16x16x128_f8f6f4 v[90:93], v[170:173], v[182:185], v[90:93] cbsz:4 blgp:4
	v_mfma_f32_16x16x128_f8f6f4 v[90:93], v[178:181], v[190:193], v[90:93] cbsz:4 blgp:4
	v_mfma_f32_16x16x128_f8f6f4 v[106:109], v[170:173], v[186:189], v[106:109] cbsz:4 blgp:4
	v_mfma_f32_16x16x128_f8f6f4 v[106:109], v[178:181], v[194:197], v[106:109] cbsz:4 blgp:4
	v_mfma_f32_16x16x128_f8f6f4 v[126:129], v[170:173], v[198:201], v[126:129] cbsz:4 blgp:4
	v_mfma_f32_16x16x128_f8f6f4 v[126:129], v[178:181], v[206:209], v[126:129] cbsz:4 blgp:4
	v_mfma_f32_16x16x128_f8f6f4 v[82:85], v[170:173], v[202:205], v[82:85] cbsz:4 blgp:4
	v_mfma_f32_16x16x128_f8f6f4 v[82:85], v[178:181], v[210:213], v[82:85] cbsz:4 blgp:4
	v_mfma_f32_16x16x128_f8f6f4 v[94:97], v[214:217], v[182:185], v[94:97] cbsz:4 blgp:4
	v_mfma_f32_16x16x128_f8f6f4 v[94:97], v[222:225], v[190:193], v[94:97] cbsz:4 blgp:4
	v_mfma_f32_16x16x128_f8f6f4 v[110:113], v[214:217], v[186:189], v[110:113] cbsz:4 blgp:4
	v_mfma_f32_16x16x128_f8f6f4 v[110:113], v[222:225], v[194:197], v[110:113] cbsz:4 blgp:4
	v_mfma_f32_16x16x128_f8f6f4 v[122:125], v[214:217], v[198:201], v[122:125] cbsz:4 blgp:4
	v_mfma_f32_16x16x128_f8f6f4 v[122:125], v[222:225], v[206:209], v[122:125] cbsz:4 blgp:4
	v_mfma_f32_16x16x128_f8f6f4 v[134:137], v[214:217], v[202:205], v[134:137] cbsz:4 blgp:4
	v_mfma_f32_16x16x128_f8f6f4 v[134:137], v[222:225], v[210:213], v[134:137] cbsz:4 blgp:4
	v_mfma_f32_16x16x128_f8f6f4 v[102:105], v[218:221], v[182:185], v[102:105] cbsz:4 blgp:4
	v_mfma_f32_16x16x128_f8f6f4 v[102:105], v[226:229], v[190:193], v[102:105] cbsz:4 blgp:4
	v_mfma_f32_16x16x128_f8f6f4 v[114:117], v[218:221], v[186:189], v[114:117] cbsz:4 blgp:4
	v_mfma_f32_16x16x128_f8f6f4 v[114:117], v[226:229], v[194:197], v[114:117] cbsz:4 blgp:4
	v_mfma_f32_16x16x128_f8f6f4 v[130:133], v[218:221], v[198:201], v[130:133] cbsz:4 blgp:4
	v_mfma_f32_16x16x128_f8f6f4 v[130:133], v[226:229], v[206:209], v[130:133] cbsz:4 blgp:4
	v_mfma_f32_16x16x128_f8f6f4 v[142:145], v[218:221], v[202:205], v[142:145] cbsz:4 blgp:4
	v_mfma_f32_16x16x128_f8f6f4 v[142:145], v[226:229], v[210:213], v[142:145] cbsz:4 blgp:4
	s_setprio 0
	s_andn2_b64 vcc, exec, s[34:35]
	s_barrier
	s_cbranch_vccnz .LBB4_4
	s_ashr_i32 s29, s28, 31
	s_lshl_b64 s[42:43], s[28:29], 10
	s_add_u32 s42, s10, s42
	s_addc_u32 s43, s11, s43
	s_add_u32 s29, s40, 0x200
	s_addc_u32 s78, s41, 0
	s_add_u32 s79, s38, 0x200
	s_addc_u32 s80, s39, 0
	s_add_u32 s38, s81, 0x180
	s_addc_u32 s39, s82, 0
	s_mov_b32 s81, 4
	s_cmp_eq_u32 s63, s81
	s_cselect_b64 s[40:41], -1, 0
	s_cmp_lg_u32 s63, s81
	s_cbranch_scc1 .LBB4_15

.LBB4_15:
	ds_read_b128 v[166:169], v161
	ds_read_b128 v[170:173], v161 offset:2048
	ds_read_b128 v[174:177], v162
	ds_read_b128 v[178:181], v162 offset:2048
	s_and_b64 s[40:41], s[40:41], exec
	s_cselect_b32 s46, s36, s29
	s_cselect_b32 s47, s37, s78
	s_cselect_b32 s49, s5, s80
	s_cselect_b32 s48, s4, s79
	s_add_u32 s44, s46, 0x80
	s_addc_u32 s45, s47, 0
	s_add_u32 s40, s48, 0x80
	s_addc_u32 s41, s49, 0
	ds_read_b128 v[182:185], v163
	ds_read_b128 v[186:189], v163 offset:2048
	ds_read_b128 v[190:193], v164
	ds_read_b128 v[194:197], v164 offset:2048
	ds_read_b128 v[198:201], v163 offset:4096
	ds_read_b128 v[202:205], v163 offset:6144
	ds_read_b128 v[206:209], v164 offset:4096
	ds_read_b128 v[210:213], v164 offset:6144
	s_mov_b32 m0, s70
	s_nop 0
	global_load_lds_dwordx4 v146, s[38:39]
	s_mov_b32 m0, s71
	s_nop 0
	global_load_lds_dwordx4 v150, s[38:39]
	s_waitcnt lgkmcnt(8)
	ds_read_b128 v[214:217], v161 offset:16384
	ds_read_b128 v[218:221], v161 offset:18432
	ds_read_b128 v[222:225], v162 offset:16384
	ds_read_b128 v[226:229], v162 offset:18432
	s_waitcnt vmcnt(8)
	s_waitcnt lgkmcnt(0)
	s_barrier
	s_waitcnt lgkmcnt(0)
	s_setprio 1
	v_mfma_f32_16x16x128_f8f6f4 v[18:21], v[166:169], v[182:185], v[18:21] cbsz:4 blgp:4
	v_mfma_f32_16x16x128_f8f6f4 v[18:21], v[174:177], v[190:193], v[18:21] cbsz:4 blgp:4
	v_mfma_f32_16x16x128_f8f6f4 v[26:29], v[166:169], v[186:189], v[26:29] cbsz:4 blgp:4
	v_mfma_f32_16x16x128_f8f6f4 v[26:29], v[174:177], v[194:197], v[26:29] cbsz:4 blgp:4
	v_mfma_f32_16x16x128_f8f6f4 v[34:37], v[166:169], v[198:201], v[34:37] cbsz:4 blgp:4
	v_mfma_f32_16x16x128_f8f6f4 v[34:37], v[174:177], v[206:209], v[34:37] cbsz:4 blgp:4
	v_mfma_f32_16x16x128_f8f6f4 v[42:45], v[166:169], v[202:205], v[42:45] cbsz:4 blgp:4
	v_mfma_f32_16x16x128_f8f6f4 v[42:45], v[174:177], v[210:213], v[42:45] cbsz:4 blgp:4
	v_mfma_f32_16x16x128_f8f6f4 v[22:25], v[170:173], v[182:185], v[22:25] cbsz:4 blgp:4
	v_mfma_f32_16x16x128_f8f6f4 v[22:25], v[178:181], v[190:193], v[22:25] cbsz:4 blgp:4
	v_mfma_f32_16x16x128_f8f6f4 v[30:33], v[170:173], v[186:189], v[30:33] cbsz:4 blgp:4
	v_mfma_f32_16x16x128_f8f6f4 v[30:33], v[178:181], v[194:197], v[30:33] cbsz:4 blgp:4
	v_mfma_f32_16x16x128_f8f6f4 v[38:41], v[170:173], v[198:201], v[38:41] cbsz:4 blgp:4
	v_mfma_f32_16x16x128_f8f6f4 v[38:41], v[178:181], v[206:209], v[38:41] cbsz:4 blgp:4
	v_mfma_f32_16x16x128_f8f6f4 v[46:49], v[170:173], v[202:205], v[46:49] cbsz:4 blgp:4
	v_mfma_f32_16x16x128_f8f6f4 v[46:49], v[178:181], v[210:213], v[46:49] cbsz:4 blgp:4
	v_mfma_f32_16x16x128_f8f6f4 v[50:53], v[214:217], v[182:185], v[50:53] cbsz:4 blgp:4
	v_mfma_f32_16x16x128_f8f6f4 v[50:53], v[222:225], v[190:193], v[50:53] cbsz:4 blgp:4
	v_mfma_f32_16x16x128_f8f6f4 v[58:61], v[214:217], v[186:189], v[58:61] cbsz:4 blgp:4
	v_mfma_f32_16x16x128_f8f6f4 v[58:61], v[222:225], v[194:197], v[58:61] cbsz:4 blgp:4
	v_mfma_f32_16x16x128_f8f6f4 v[66:69], v[214:217], v[198:201], v[66:69] cbsz:4 blgp:4
	v_mfma_f32_16x16x128_f8f6f4 v[66:69], v[222:225], v[206:209], v[66:69] cbsz:4 blgp:4
	v_mfma_f32_16x16x128_f8f6f4 v[74:77], v[214:217], v[202:205], v[74:77] cbsz:4 blgp:4
	v_mfma_f32_16x16x128_f8f6f4 v[74:77], v[222:225], v[210:213], v[74:77] cbsz:4 blgp:4
	v_mfma_f32_16x16x128_f8f6f4 v[54:57], v[218:221], v[182:185], v[54:57] cbsz:4 blgp:4
	v_mfma_f32_16x16x128_f8f6f4 v[54:57], v[226:229], v[190:193], v[54:57] cbsz:4 blgp:4
	v_mfma_f32_16x16x128_f8f6f4 v[62:65], v[218:221], v[186:189], v[62:65] cbsz:4 blgp:4
	v_mfma_f32_16x16x128_f8f6f4 v[62:65], v[226:229], v[194:197], v[62:65] cbsz:4 blgp:4
	v_mfma_f32_16x16x128_f8f6f4 v[70:73], v[218:221], v[198:201], v[70:73] cbsz:4 blgp:4
	v_mfma_f32_16x16x128_f8f6f4 v[70:73], v[226:229], v[206:209], v[70:73] cbsz:4 blgp:4
	v_mfma_f32_16x16x128_f8f6f4 v[78:81], v[218:221], v[202:205], v[78:81] cbsz:4 blgp:4
	v_mfma_f32_16x16x128_f8f6f4 v[78:81], v[226:229], v[210:213], v[78:81] cbsz:4 blgp:4
	s_setprio 0
	s_barrier
	s_mov_b32 m0, s55
	s_nop 0
	global_load_lds_dwordx4 v148, s[48:49]
	s_mov_b32 m0, s56
	s_nop 0
	global_load_lds_dwordx4 v152, s[48:49]
	ds_read_b128 v[182:185], v163 offset:16384
	ds_read_b128 v[186:189], v163 offset:18432
	ds_read_b128 v[190:193], v164 offset:16384
	ds_read_b128 v[194:197], v164 offset:18432
	ds_read_b128 v[198:201], v163 offset:20480
	ds_read_b128 v[202:205], v163 offset:22528
	ds_read_b128 v[206:209], v164 offset:20480
	ds_read_b128 v[210:213], v164 offset:22528
	s_mov_b32 m0, s54
	s_nop 0
	global_load_lds_dwordx4 v146, s[46:47]
	s_mov_b32 m0, s57
	s_nop 0
	global_load_lds_dwordx4 v150, s[46:47]
	s_add_u32 s48, s48, s24
	s_addc_u32 s49, s49, s25
	s_mov_b32 m0, s58
	s_nop 0
	global_load_lds_dwordx4 v148, s[48:49]
	s_mov_b32 m0, s59
	s_nop 0
	global_load_lds_dwordx4 v152, s[48:49]
	s_waitcnt vmcnt(8)
	s_waitcnt lgkmcnt(0)
	s_barrier
	s_setprio 1
	v_mfma_f32_16x16x128_f8f6f4 v[86:89], v[166:169], v[182:185], v[86:89] cbsz:4 blgp:4
	v_mfma_f32_16x16x128_f8f6f4 v[86:89], v[174:177], v[190:193], v[86:89] cbsz:4 blgp:4
	v_mfma_f32_16x16x128_f8f6f4 v[98:101], v[166:169], v[186:189], v[98:101] cbsz:4 blgp:4
	v_mfma_f32_16x16x128_f8f6f4 v[98:101], v[174:177], v[194:197], v[98:101] cbsz:4 blgp:4
	v_mfma_f32_16x16x128_f8f6f4 v[118:121], v[166:169], v[198:201], v[118:121] cbsz:4 blgp:4
	v_mfma_f32_16x16x128_f8f6f4 v[118:121], v[174:177], v[206:209], v[118:121] cbsz:4 blgp:4
	v_mfma_f32_16x16x128_f8f6f4 v[138:141], v[166:169], v[202:205], v[138:141] cbsz:4 blgp:4
	v_mfma_f32_16x16x128_f8f6f4 v[138:141], v[174:177], v[210:213], v[138:141] cbsz:4 blgp:4
	v_mfma_f32_16x16x128_f8f6f4 v[90:93], v[170:173], v[182:185], v[90:93] cbsz:4 blgp:4
	v_mfma_f32_16x16x128_f8f6f4 v[90:93], v[178:181], v[190:193], v[90:93] cbsz:4 blgp:4
	v_mfma_f32_16x16x128_f8f6f4 v[106:109], v[170:173], v[186:189], v[106:109] cbsz:4 blgp:4
	v_mfma_f32_16x16x128_f8f6f4 v[106:109], v[178:181], v[194:197], v[106:109] cbsz:4 blgp:4
	v_mfma_f32_16x16x128_f8f6f4 v[126:129], v[170:173], v[198:201], v[126:129] cbsz:4 blgp:4
	v_mfma_f32_16x16x128_f8f6f4 v[126:129], v[178:181], v[206:209], v[126:129] cbsz:4 blgp:4
	v_mfma_f32_16x16x128_f8f6f4 v[82:85], v[170:173], v[202:205], v[82:85] cbsz:4 blgp:4
	v_mfma_f32_16x16x128_f8f6f4 v[82:85], v[178:181], v[210:213], v[82:85] cbsz:4 blgp:4
	v_mfma_f32_16x16x128_f8f6f4 v[94:97], v[214:217], v[182:185], v[94:97] cbsz:4 blgp:4
	v_mfma_f32_16x16x128_f8f6f4 v[94:97], v[222:225], v[190:193], v[94:97] cbsz:4 blgp:4
	v_mfma_f32_16x16x128_f8f6f4 v[110:113], v[214:217], v[186:189], v[110:113] cbsz:4 blgp:4
	v_mfma_f32_16x16x128_f8f6f4 v[110:113], v[222:225], v[194:197], v[110:113] cbsz:4 blgp:4
	v_mfma_f32_16x16x128_f8f6f4 v[122:125], v[214:217], v[198:201], v[122:125] cbsz:4 blgp:4
	v_mfma_f32_16x16x128_f8f6f4 v[122:125], v[222:225], v[206:209], v[122:125] cbsz:4 blgp:4
	v_mfma_f32_16x16x128_f8f6f4 v[134:137], v[214:217], v[202:205], v[134:137] cbsz:4 blgp:4
	v_mfma_f32_16x16x128_f8f6f4 v[134:137], v[222:225], v[210:213], v[134:137] cbsz:4 blgp:4
	v_mfma_f32_16x16x128_f8f6f4 v[102:105], v[218:221], v[182:185], v[102:105] cbsz:4 blgp:4
	v_mfma_f32_16x16x128_f8f6f4 v[102:105], v[226:229], v[190:193], v[102:105] cbsz:4 blgp:4
	v_mfma_f32_16x16x128_f8f6f4 v[114:117], v[218:221], v[186:189], v[114:117] cbsz:4 blgp:4
	v_mfma_f32_16x16x128_f8f6f4 v[114:117], v[226:229], v[194:197], v[114:117] cbsz:4 blgp:4
	v_mfma_f32_16x16x128_f8f6f4 v[130:133], v[218:221], v[198:201], v[130:133] cbsz:4 blgp:4
	v_mfma_f32_16x16x128_f8f6f4 v[130:133], v[226:229], v[206:209], v[130:133] cbsz:4 blgp:4
	v_mfma_f32_16x16x128_f8f6f4 v[142:145], v[218:221], v[202:205], v[142:145] cbsz:4 blgp:4
	v_mfma_f32_16x16x128_f8f6f4 v[142:145], v[226:229], v[210:213], v[142:145] cbsz:4 blgp:4
	s_setprio 0
	s_barrier
	ds_read_b128 v[166:169], v161 offset:32768
	ds_read_b128 v[170:173], v161 offset:34816
	ds_read_b128 v[174:177], v162 offset:32768
	ds_read_b128 v[178:181], v162 offset:34816
	ds_read_b128 v[182:185], v163 offset:32768
	ds_read_b128 v[186:189], v163 offset:34816
	ds_read_b128 v[190:193], v164 offset:32768
	ds_read_b128 v[194:197], v164 offset:34816
	ds_read_b128 v[198:201], v163 offset:36864
	ds_read_b128 v[202:205], v163 offset:38912
	ds_read_b128 v[206:209], v164 offset:36864
	ds_read_b128 v[210:213], v164 offset:38912
	s_add_u32 s46, s46, s22
	s_addc_u32 s47, s47, s23
	s_mov_b32 m0, s60
	s_nop 0
	global_load_lds_dwordx4 v146, s[46:47]
	s_mov_b32 m0, s61
	s_nop 0
	global_load_lds_dwordx4 v150, s[46:47]
	s_waitcnt lgkmcnt(8)
	ds_read_b128 v[214:217], v161 offset:49152
	ds_read_b128 v[218:221], v161 offset:51200
	ds_read_b128 v[222:225], v162 offset:49152
	ds_read_b128 v[226:229], v162 offset:51200
	s_waitcnt vmcnt(8)
	s_waitcnt lgkmcnt(0)
	s_barrier
	s_waitcnt lgkmcnt(0)
	s_setprio 1
	v_mfma_f32_16x16x128_f8f6f4 v[18:21], v[166:169], v[182:185], v[18:21] cbsz:4 blgp:4
	v_mfma_f32_16x16x128_f8f6f4 v[18:21], v[174:177], v[190:193], v[18:21] cbsz:4 blgp:4
	v_mfma_f32_16x16x128_f8f6f4 v[26:29], v[166:169], v[186:189], v[26:29] cbsz:4 blgp:4
	v_mfma_f32_16x16x128_f8f6f4 v[26:29], v[174:177], v[194:197], v[26:29] cbsz:4 blgp:4
	v_mfma_f32_16x16x128_f8f6f4 v[34:37], v[166:169], v[198:201], v[34:37] cbsz:4 blgp:4
	v_mfma_f32_16x16x128_f8f6f4 v[34:37], v[174:177], v[206:209], v[34:37] cbsz:4 blgp:4
	v_mfma_f32_16x16x128_f8f6f4 v[42:45], v[166:169], v[202:205], v[42:45] cbsz:4 blgp:4
	v_mfma_f32_16x16x128_f8f6f4 v[42:45], v[174:177], v[210:213], v[42:45] cbsz:4 blgp:4
	v_mfma_f32_16x16x128_f8f6f4 v[22:25], v[170:173], v[182:185], v[22:25] cbsz:4 blgp:4
	v_mfma_f32_16x16x128_f8f6f4 v[22:25], v[178:181], v[190:193], v[22:25] cbsz:4 blgp:4
	v_mfma_f32_16x16x128_f8f6f4 v[30:33], v[170:173], v[186:189], v[30:33] cbsz:4 blgp:4
	v_mfma_f32_16x16x128_f8f6f4 v[30:33], v[178:181], v[194:197], v[30:33] cbsz:4 blgp:4
	v_mfma_f32_16x16x128_f8f6f4 v[38:41], v[170:173], v[198:201], v[38:41] cbsz:4 blgp:4
	v_mfma_f32_16x16x128_f8f6f4 v[38:41], v[178:181], v[206:209], v[38:41] cbsz:4 blgp:4
	v_mfma_f32_16x16x128_f8f6f4 v[46:49], v[170:173], v[202:205], v[46:49] cbsz:4 blgp:4
	v_mfma_f32_16x16x128_f8f6f4 v[46:49], v[178:181], v[210:213], v[46:49] cbsz:4 blgp:4
	v_mfma_f32_16x16x128_f8f6f4 v[50:53], v[214:217], v[182:185], v[50:53] cbsz:4 blgp:4
	v_mfma_f32_16x16x128_f8f6f4 v[50:53], v[222:225], v[190:193], v[50:53] cbsz:4 blgp:4
	v_mfma_f32_16x16x128_f8f6f4 v[58:61], v[214:217], v[186:189], v[58:61] cbsz:4 blgp:4
	v_mfma_f32_16x16x128_f8f6f4 v[58:61], v[222:225], v[194:197], v[58:61] cbsz:4 blgp:4
	v_mfma_f32_16x16x128_f8f6f4 v[66:69], v[214:217], v[198:201], v[66:69] cbsz:4 blgp:4
	v_mfma_f32_16x16x128_f8f6f4 v[66:69], v[222:225], v[206:209], v[66:69] cbsz:4 blgp:4
	v_mfma_f32_16x16x128_f8f6f4 v[74:77], v[214:217], v[202:205], v[74:77] cbsz:4 blgp:4
	v_mfma_f32_16x16x128_f8f6f4 v[74:77], v[222:225], v[210:213], v[74:77] cbsz:4 blgp:4
	v_mfma_f32_16x16x128_f8f6f4 v[54:57], v[218:221], v[182:185], v[54:57] cbsz:4 blgp:4
	v_mfma_f32_16x16x128_f8f6f4 v[54:57], v[226:229], v[190:193], v[54:57] cbsz:4 blgp:4
	v_mfma_f32_16x16x128_f8f6f4 v[62:65], v[218:221], v[186:189], v[62:65] cbsz:4 blgp:4
	v_mfma_f32_16x16x128_f8f6f4 v[62:65], v[226:229], v[194:197], v[62:65] cbsz:4 blgp:4
	v_mfma_f32_16x16x128_f8f6f4 v[70:73], v[218:221], v[198:201], v[70:73] cbsz:4 blgp:4
	v_mfma_f32_16x16x128_f8f6f4 v[70:73], v[226:229], v[206:209], v[70:73] cbsz:4 blgp:4
	v_mfma_f32_16x16x128_f8f6f4 v[78:81], v[218:221], v[202:205], v[78:81] cbsz:4 blgp:4
	v_mfma_f32_16x16x128_f8f6f4 v[78:81], v[226:229], v[210:213], v[78:81] cbsz:4 blgp:4
	s_setprio 0
	s_barrier
	s_mov_b32 m0, s64
	s_nop 0
	global_load_lds_dwordx4 v148, s[40:41]
	s_mov_b32 m0, s65
	s_nop 0
	global_load_lds_dwordx4 v152, s[40:41]
	ds_read_b128 v[182:185], v163 offset:49152
	ds_read_b128 v[186:189], v163 offset:51200
	ds_read_b128 v[190:193], v164 offset:49152
	ds_read_b128 v[194:197], v164 offset:51200
	ds_read_b128 v[198:201], v163 offset:53248
	ds_read_b128 v[202:205], v163 offset:55296
	ds_read_b128 v[206:209], v164 offset:53248
	ds_read_b128 v[210:213], v164 offset:55296
	s_mov_b32 m0, s66
	s_nop 0
	global_load_lds_dwordx4 v146, s[44:45]
	s_mov_b32 m0, s67
	s_nop 0
	global_load_lds_dwordx4 v150, s[44:45]
	s_add_u32 s40, s40, s24
	s_addc_u32 s41, s41, s25
	s_mov_b32 m0, s68
	s_nop 0
	global_load_lds_dwordx4 v148, s[40:41]
	s_mov_b32 m0, s69
	s_nop 0
	global_load_lds_dwordx4 v152, s[40:41]
	s_waitcnt vmcnt(8)
	s_waitcnt lgkmcnt(0)
	s_barrier
	s_setprio 1
	v_mfma_f32_16x16x128_f8f6f4 v[86:89], v[166:169], v[182:185], v[86:89] cbsz:4 blgp:4
	v_mfma_f32_16x16x128_f8f6f4 v[86:89], v[174:177], v[190:193], v[86:89] cbsz:4 blgp:4
	v_mfma_f32_16x16x128_f8f6f4 v[98:101], v[166:169], v[186:189], v[98:101] cbsz:4 blgp:4
	v_mfma_f32_16x16x128_f8f6f4 v[98:101], v[174:177], v[194:197], v[98:101] cbsz:4 blgp:4
	v_mfma_f32_16x16x128_f8f6f4 v[118:121], v[166:169], v[198:201], v[118:121] cbsz:4 blgp:4
	v_mfma_f32_16x16x128_f8f6f4 v[118:121], v[174:177], v[206:209], v[118:121] cbsz:4 blgp:4
	v_mfma_f32_16x16x128_f8f6f4 v[138:141], v[166:169], v[202:205], v[138:141] cbsz:4 blgp:4
	v_mfma_f32_16x16x128_f8f6f4 v[138:141], v[174:177], v[210:213], v[138:141] cbsz:4 blgp:4
	v_mfma_f32_16x16x128_f8f6f4 v[90:93], v[170:173], v[182:185], v[90:93] cbsz:4 blgp:4
	v_mfma_f32_16x16x128_f8f6f4 v[90:93], v[178:181], v[190:193], v[90:93] cbsz:4 blgp:4
	v_mfma_f32_16x16x128_f8f6f4 v[106:109], v[170:173], v[186:189], v[106:109] cbsz:4 blgp:4
	v_mfma_f32_16x16x128_f8f6f4 v[106:109], v[178:181], v[194:197], v[106:109] cbsz:4 blgp:4
	v_mfma_f32_16x16x128_f8f6f4 v[126:129], v[170:173], v[198:201], v[126:129] cbsz:4 blgp:4
	v_mfma_f32_16x16x128_f8f6f4 v[126:129], v[178:181], v[206:209], v[126:129] cbsz:4 blgp:4
	v_mfma_f32_16x16x128_f8f6f4 v[82:85], v[170:173], v[202:205], v[82:85] cbsz:4 blgp:4
	v_mfma_f32_16x16x128_f8f6f4 v[82:85], v[178:181], v[210:213], v[82:85] cbsz:4 blgp:4
	v_mfma_f32_16x16x128_f8f6f4 v[94:97], v[214:217], v[182:185], v[94:97] cbsz:4 blgp:4
	v_mfma_f32_16x16x128_f8f6f4 v[94:97], v[222:225], v[190:193], v[94:97] cbsz:4 blgp:4
	v_mfma_f32_16x16x128_f8f6f4 v[110:113], v[214:217], v[186:189], v[110:113] cbsz:4 blgp:4
	v_mfma_f32_16x16x128_f8f6f4 v[110:113], v[222:225], v[194:197], v[110:113] cbsz:4 blgp:4
	v_mfma_f32_16x16x128_f8f6f4 v[122:125], v[214:217], v[198:201], v[122:125] cbsz:4 blgp:4
	v_mfma_f32_16x16x128_f8f6f4 v[122:125], v[222:225], v[206:209], v[122:125] cbsz:4 blgp:4
	v_mfma_f32_16x16x128_f8f6f4 v[134:137], v[214:217], v[202:205], v[134:137] cbsz:4 blgp:4
	v_mfma_f32_16x16x128_f8f6f4 v[134:137], v[222:225], v[210:213], v[134:137] cbsz:4 blgp:4
	v_mfma_f32_16x16x128_f8f6f4 v[102:105], v[218:221], v[182:185], v[102:105] cbsz:4 blgp:4
	v_mfma_f32_16x16x128_f8f6f4 v[102:105], v[226:229], v[190:193], v[102:105] cbsz:4 blgp:4
	v_mfma_f32_16x16x128_f8f6f4 v[114:117], v[218:221], v[186:189], v[114:117] cbsz:4 blgp:4
	v_mfma_f32_16x16x128_f8f6f4 v[114:117], v[226:229], v[194:197], v[114:117] cbsz:4 blgp:4
	v_mfma_f32_16x16x128_f8f6f4 v[130:133], v[218:221], v[198:201], v[130:133] cbsz:4 blgp:4
	v_mfma_f32_16x16x128_f8f6f4 v[130:133], v[226:229], v[206:209], v[130:133] cbsz:4 blgp:4
	v_mfma_f32_16x16x128_f8f6f4 v[142:145], v[218:221], v[202:205], v[142:145] cbsz:4 blgp:4
	v_mfma_f32_16x16x128_f8f6f4 v[142:145], v[226:229], v[210:213], v[142:145] cbsz:4 blgp:4
	s_setprio 0
	s_add_i32 s40, s81, 2
	s_add_u32 s29, s29, 0x100
	s_addc_u32 s78, s78, 0
	s_add_u32 s79, s79, 0x100
	s_addc_u32 s80, s80, 0
	s_add_u32 s38, s38, 0x100
	s_addc_u32 s39, s39, 0
	s_cmp_ge_i32 s81, s63
	s_barrier
	s_cbranch_scc1 .LBB4_4
	s_mov_b32 s81, s40
	s_cmp_eq_u32 s63, s81
	s_cselect_b64 s[40:41], -1, 0
	s_cmp_lg_u32 s63, s81
	s_cbranch_scc0 .LBB4_14
	s_branch .LBB4_15

.Lrs_a_5:
	s_add_u32 s82, s42, s22
	s_addc_u32 s83, s43, s23
	s_add_u32 s29, s42, 0x100
	s_addc_u32 s46, s43, 0
	s_and_b64 s[44:45], s[14:15], exec
	ds_read_b128 v[82:85], v163
	ds_read_b128 v[94:97], v163 offset:2048
	ds_read_b128 v[102:105], v164
	ds_read_b128 v[110:113], v164 offset:2048
	s_cselect_b32 s49, s39, s46
	s_cselect_b32 s48, s38, s29
	s_add_u32 s29, s40, 0x100
	s_addc_u32 s46, s41, 0
	s_and_b64 s[44:45], s[14:15], exec
	s_cselect_b32 s51, s5, s46
	s_cselect_b32 s50, s4, s29
	s_add_u32 s46, s48, 0x80
	s_addc_u32 s47, s49, 0
	s_add_u32 s44, s50, 0x80
	s_addc_u32 s45, s51, 0
	ds_read_b128 v[58:61], v165
	ds_read_b128 v[66:69], v165 offset:2048
	ds_read_b128 v[62:65], v166
	ds_read_b128 v[70:73], v166 offset:2048
	ds_read_b128 v[74:77], v165 offset:4096
	ds_read_b128 v[86:89], v165 offset:6144
	ds_read_b128 v[78:81], v166 offset:4096
	ds_read_b128 v[90:93], v166 offset:6144
	s_add_u32 s80, s82, 0x80
	s_addc_u32 s81, s83, 0
	s_mov_b32 m0, s71
	s_nop 0
	global_load_lds_dwordx4 v146, s[80:81]
	s_mov_b32 m0, s72
	s_nop 0
	global_load_lds_dwordx4 v150, s[80:81]
	s_waitcnt lgkmcnt(8)
	ds_read_b128 v[142:145], v163 offset:16384
	ds_read_b128 v[156:159], v163 offset:18432
	ds_read_b128 v[168:171], v164 offset:16384
	ds_read_b128 v[172:175], v164 offset:18432
	s_waitcnt vmcnt(8)
	s_waitcnt lgkmcnt(0)
	s_barrier
	s_waitcnt lgkmcnt(0)
	s_waitcnt vmcnt(16)
	v_mov_b32_e32 v1, v0
	v_pk_mul_f32 v[16:17], v[0:1], v[16:17]
	v_pk_mul_f32 v[14:15], v[154:155], v[14:15]
	v_pk_mul_f32 v[12:13], v[0:1], v[12:13]
	v_pk_mul_f32 v[10:11], v[154:155], v[10:11]
	v_pk_mul_f32 v[8:9], v[0:1], v[8:9]
	v_pk_mul_f32 v[6:7], v[154:155], v[6:7]
	v_pk_mul_f32 v[4:5], v[0:1], v[4:5]
	v_pk_mul_f32 v[2:3], v[154:155], v[2:3]
	s_setprio 1
	v_mfma_f32_16x16x128_f8f6f4 v[18:21], v[82:85], v[58:61], v[14:17] cbsz:4 blgp:4
	v_mfma_f32_16x16x128_f8f6f4 v[18:21], v[102:105], v[62:65], v[18:21] cbsz:4 blgp:4
	v_mfma_f32_16x16x128_f8f6f4 v[26:29], v[82:85], v[66:69], v[14:17] cbsz:4 blgp:4
	v_mfma_f32_16x16x128_f8f6f4 v[26:29], v[102:105], v[70:73], v[26:29] cbsz:4 blgp:4
	v_mfma_f32_16x16x128_f8f6f4 v[34:37], v[82:85], v[74:77], v[14:17] cbsz:4 blgp:4
	v_mfma_f32_16x16x128_f8f6f4 v[34:37], v[102:105], v[78:81], v[34:37] cbsz:4 blgp:4
	v_mfma_f32_16x16x128_f8f6f4 v[42:45], v[82:85], v[86:89], v[14:17] cbsz:4 blgp:4
	v_mfma_f32_16x16x128_f8f6f4 v[42:45], v[102:105], v[90:93], v[42:45] cbsz:4 blgp:4
	v_mfma_f32_16x16x128_f8f6f4 v[22:25], v[94:97], v[58:61], v[10:13] cbsz:4 blgp:4
	v_mfma_f32_16x16x128_f8f6f4 v[22:25], v[110:113], v[62:65], v[22:25] cbsz:4 blgp:4
	v_mfma_f32_16x16x128_f8f6f4 v[30:33], v[94:97], v[66:69], v[10:13] cbsz:4 blgp:4
	v_mfma_f32_16x16x128_f8f6f4 v[30:33], v[110:113], v[70:73], v[30:33] cbsz:4 blgp:4
	v_mfma_f32_16x16x128_f8f6f4 v[38:41], v[94:97], v[74:77], v[10:13] cbsz:4 blgp:4
	v_mfma_f32_16x16x128_f8f6f4 v[38:41], v[110:113], v[78:81], v[38:41] cbsz:4 blgp:4
	v_mfma_f32_16x16x128_f8f6f4 v[46:49], v[94:97], v[86:89], v[10:13] cbsz:4 blgp:4
	v_mfma_f32_16x16x128_f8f6f4 v[46:49], v[110:113], v[90:93], v[46:49] cbsz:4 blgp:4
	v_mfma_f32_16x16x128_f8f6f4 v[50:53], v[142:145], v[58:61], v[6:9] cbsz:4 blgp:4
	v_mfma_f32_16x16x128_f8f6f4 v[50:53], v[168:171], v[62:65], v[50:53] cbsz:4 blgp:4
	v_mfma_f32_16x16x128_f8f6f4 v[54:57], v[156:159], v[58:61], v[2:5] cbsz:4 blgp:4
	v_mfma_f32_16x16x128_f8f6f4 v[54:57], v[172:175], v[62:65], v[54:57] cbsz:4 blgp:4
	v_mfma_f32_16x16x128_f8f6f4 v[58:61], v[142:145], v[66:69], v[6:9] cbsz:4 blgp:4
	v_mfma_f32_16x16x128_f8f6f4 v[58:61], v[168:171], v[70:73], v[58:61] cbsz:4 blgp:4
	v_mfma_f32_16x16x128_f8f6f4 v[62:65], v[156:159], v[66:69], v[2:5] cbsz:4 blgp:4
	v_mfma_f32_16x16x128_f8f6f4 v[62:65], v[172:175], v[70:73], v[62:65] cbsz:4 blgp:4
	v_mfma_f32_16x16x128_f8f6f4 v[66:69], v[142:145], v[74:77], v[6:9] cbsz:4 blgp:4
	v_mfma_f32_16x16x128_f8f6f4 v[66:69], v[168:171], v[78:81], v[66:69] cbsz:4 blgp:4
	v_mfma_f32_16x16x128_f8f6f4 v[70:73], v[156:159], v[74:77], v[2:5] cbsz:4 blgp:4
	v_mfma_f32_16x16x128_f8f6f4 v[70:73], v[172:175], v[78:81], v[70:73] cbsz:4 blgp:4
	v_mfma_f32_16x16x128_f8f6f4 v[74:77], v[142:145], v[86:89], v[6:9] cbsz:4 blgp:4
	v_mfma_f32_16x16x128_f8f6f4 v[74:77], v[168:171], v[90:93], v[74:77] cbsz:4 blgp:4
	v_mfma_f32_16x16x128_f8f6f4 v[78:81], v[156:159], v[86:89], v[2:5] cbsz:4 blgp:4
	v_mfma_f32_16x16x128_f8f6f4 v[78:81], v[172:175], v[90:93], v[78:81] cbsz:4 blgp:4
	s_setprio 0
	s_barrier
	s_mov_b32 m0, s56
	s_nop 0
	global_load_lds_dwordx4 v148, s[50:51]
	s_mov_b32 m0, s57
	s_nop 0
	global_load_lds_dwordx4 v152, s[50:51]
	ds_read_b128 v[114:117], v165 offset:16384
	ds_read_b128 v[122:125], v165 offset:18432
	ds_read_b128 v[130:133], v166 offset:16384
	ds_read_b128 v[134:137], v166 offset:18432
	ds_read_b128 v[176:179], v165 offset:20480
	ds_read_b128 v[180:183], v165 offset:22528
	ds_read_b128 v[184:187], v166 offset:20480
	ds_read_b128 v[188:191], v166 offset:22528
	s_mov_b32 m0, s55
	s_nop 0
	global_load_lds_dwordx4 v146, s[48:49]
	s_mov_b32 m0, s58
	s_nop 0
	global_load_lds_dwordx4 v150, s[48:49]
	s_add_u32 s50, s50, s24
	s_addc_u32 s51, s51, s25
	s_mov_b32 m0, s59
	s_nop 0
	global_load_lds_dwordx4 v148, s[50:51]
	s_mov_b32 m0, s60
	s_nop 0
	global_load_lds_dwordx4 v152, s[50:51]
	s_waitcnt vmcnt(8)
	s_waitcnt lgkmcnt(0)
	s_barrier
	s_setprio 1
	v_mfma_f32_16x16x128_f8f6f4 v[86:89], v[82:85], v[114:117], v[14:17] cbsz:4 blgp:4
	v_mfma_f32_16x16x128_f8f6f4 v[86:89], v[102:105], v[130:133], v[86:89] cbsz:4 blgp:4
	v_mfma_f32_16x16x128_f8f6f4 v[98:101], v[82:85], v[122:125], v[14:17] cbsz:4 blgp:4
	v_mfma_f32_16x16x128_f8f6f4 v[98:101], v[102:105], v[134:137], v[98:101] cbsz:4 blgp:4
	v_mfma_f32_16x16x128_f8f6f4 v[118:121], v[82:85], v[176:179], v[14:17] cbsz:4 blgp:4
	v_mfma_f32_16x16x128_f8f6f4 v[118:121], v[102:105], v[184:187], v[118:121] cbsz:4 blgp:4
	v_mfma_f32_16x16x128_f8f6f4 v[138:141], v[82:85], v[180:183], v[14:17] cbsz:4 blgp:4
	v_mfma_f32_16x16x128_f8f6f4 v[138:141], v[102:105], v[188:191], v[138:141] cbsz:4 blgp:4
	v_mfma_f32_16x16x128_f8f6f4 v[90:93], v[94:97], v[114:117], v[10:13] cbsz:4 blgp:4
	v_mfma_f32_16x16x128_f8f6f4 v[90:93], v[110:113], v[130:133], v[90:93] cbsz:4 blgp:4
	v_mfma_f32_16x16x128_f8f6f4 v[106:109], v[94:97], v[122:125], v[10:13] cbsz:4 blgp:4
	v_mfma_f32_16x16x128_f8f6f4 v[106:109], v[110:113], v[134:137], v[106:109] cbsz:4 blgp:4
	v_mfma_f32_16x16x128_f8f6f4 v[126:129], v[94:97], v[176:179], v[10:13] cbsz:4 blgp:4
	v_mfma_f32_16x16x128_f8f6f4 v[126:129], v[110:113], v[184:187], v[126:129] cbsz:4 blgp:4
	v_mfma_f32_16x16x128_f8f6f4 v[82:85], v[94:97], v[180:183], v[10:13] cbsz:4 blgp:4
	v_mfma_f32_16x16x128_f8f6f4 v[82:85], v[110:113], v[188:191], v[82:85] cbsz:4 blgp:4
	v_mfma_f32_16x16x128_f8f6f4 v[94:97], v[142:145], v[114:117], v[6:9] cbsz:4 blgp:4
	v_mfma_f32_16x16x128_f8f6f4 v[94:97], v[168:171], v[130:133], v[94:97] cbsz:4 blgp:4
	v_mfma_f32_16x16x128_f8f6f4 v[102:105], v[156:159], v[114:117], v[2:5] cbsz:4 blgp:4
	v_mfma_f32_16x16x128_f8f6f4 v[102:105], v[172:175], v[130:133], v[102:105] cbsz:4 blgp:4
	v_mfma_f32_16x16x128_f8f6f4 v[110:113], v[142:145], v[122:125], v[6:9] cbsz:4 blgp:4
	v_mfma_f32_16x16x128_f8f6f4 v[110:113], v[168:171], v[134:137], v[110:113] cbsz:4 blgp:4
	v_mfma_f32_16x16x128_f8f6f4 v[114:117], v[156:159], v[122:125], v[2:5] cbsz:4 blgp:4
	v_mfma_f32_16x16x128_f8f6f4 v[114:117], v[172:175], v[134:137], v[114:117] cbsz:4 blgp:4
	v_mfma_f32_16x16x128_f8f6f4 v[122:125], v[142:145], v[176:179], v[6:9] cbsz:4 blgp:4
	v_mfma_f32_16x16x128_f8f6f4 v[122:125], v[168:171], v[184:187], v[122:125] cbsz:4 blgp:4
	v_mfma_f32_16x16x128_f8f6f4 v[130:133], v[156:159], v[176:179], v[2:5] cbsz:4 blgp:4
	v_mfma_f32_16x16x128_f8f6f4 v[130:133], v[172:175], v[184:187], v[130:133] cbsz:4 blgp:4
	v_mfma_f32_16x16x128_f8f6f4 v[134:137], v[142:145], v[180:183], v[6:9] cbsz:4 blgp:4
	v_mfma_f32_16x16x128_f8f6f4 v[134:137], v[168:171], v[188:191], v[134:137] cbsz:4 blgp:4
	v_mfma_f32_16x16x128_f8f6f4 v[142:145], v[156:159], v[180:183], v[2:5] cbsz:4 blgp:4
	v_mfma_f32_16x16x128_f8f6f4 v[142:145], v[172:175], v[188:191], v[142:145] cbsz:4 blgp:4
	s_setprio 0
	s_barrier
	ds_read_b128 v[156:159], v163 offset:32768
	ds_read_b128 v[168:171], v163 offset:34816
	ds_read_b128 v[172:175], v164 offset:32768
	ds_read_b128 v[176:179], v164 offset:34816
	ds_read_b128 v[180:183], v165 offset:32768
	ds_read_b128 v[184:187], v165 offset:34816
	ds_read_b128 v[188:191], v166 offset:32768
	ds_read_b128 v[192:195], v166 offset:34816
	ds_read_b128 v[196:199], v165 offset:36864
	ds_read_b128 v[200:203], v165 offset:38912
	ds_read_b128 v[204:207], v166 offset:36864
	ds_read_b128 v[208:211], v166 offset:38912
	s_add_u32 s48, s48, s22
	s_addc_u32 s49, s49, s23
	s_mov_b32 m0, s61
	s_nop 0
	global_load_lds_dwordx4 v146, s[48:49]
	s_mov_b32 m0, s62
	s_nop 0
	global_load_lds_dwordx4 v150, s[48:49]
	s_waitcnt lgkmcnt(8)
	ds_read_b128 v[212:215], v163 offset:49152
	ds_read_b128 v[216:219], v163 offset:51200
	ds_read_b128 v[220:223], v164 offset:49152
	ds_read_b128 v[224:227], v164 offset:51200
	s_waitcnt vmcnt(8)
	s_waitcnt lgkmcnt(0)
	s_barrier
	s_waitcnt lgkmcnt(0)
	s_setprio 1
	v_mfma_f32_16x16x128_f8f6f4 v[18:21], v[156:159], v[180:183], v[18:21] cbsz:4 blgp:4
	v_mfma_f32_16x16x128_f8f6f4 v[18:21], v[172:175], v[188:191], v[18:21] cbsz:4 blgp:4
	v_mfma_f32_16x16x128_f8f6f4 v[26:29], v[156:159], v[184:187], v[26:29] cbsz:4 blgp:4
	v_mfma_f32_16x16x128_f8f6f4 v[26:29], v[172:175], v[192:195], v[26:29] cbsz:4 blgp:4
	v_mfma_f32_16x16x128_f8f6f4 v[34:37], v[156:159], v[196:199], v[34:37] cbsz:4 blgp:4
	v_mfma_f32_16x16x128_f8f6f4 v[34:37], v[172:175], v[204:207], v[34:37] cbsz:4 blgp:4
	v_mfma_f32_16x16x128_f8f6f4 v[42:45], v[156:159], v[200:203], v[42:45] cbsz:4 blgp:4
	v_mfma_f32_16x16x128_f8f6f4 v[42:45], v[172:175], v[208:211], v[42:45] cbsz:4 blgp:4
	v_mfma_f32_16x16x128_f8f6f4 v[22:25], v[168:171], v[180:183], v[22:25] cbsz:4 blgp:4
	v_mfma_f32_16x16x128_f8f6f4 v[22:25], v[176:179], v[188:191], v[22:25] cbsz:4 blgp:4
	v_mfma_f32_16x16x128_f8f6f4 v[30:33], v[168:171], v[184:187], v[30:33] cbsz:4 blgp:4
	v_mfma_f32_16x16x128_f8f6f4 v[30:33], v[176:179], v[192:195], v[30:33] cbsz:4 blgp:4
	v_mfma_f32_16x16x128_f8f6f4 v[38:41], v[168:171], v[196:199], v[38:41] cbsz:4 blgp:4
	v_mfma_f32_16x16x128_f8f6f4 v[38:41], v[176:179], v[204:207], v[38:41] cbsz:4 blgp:4
	v_mfma_f32_16x16x128_f8f6f4 v[46:49], v[168:171], v[200:203], v[46:49] cbsz:4 blgp:4
	v_mfma_f32_16x16x128_f8f6f4 v[46:49], v[176:179], v[208:211], v[46:49] cbsz:4 blgp:4
	v_mfma_f32_16x16x128_f8f6f4 v[50:53], v[212:215], v[180:183], v[50:53] cbsz:4 blgp:4
	v_mfma_f32_16x16x128_f8f6f4 v[50:53], v[220:223], v[188:191], v[50:53] cbsz:4 blgp:4
	v_mfma_f32_16x16x128_f8f6f4 v[58:61], v[212:215], v[184:187], v[58:61] cbsz:4 blgp:4
	v_mfma_f32_16x16x128_f8f6f4 v[58:61], v[220:223], v[192:195], v[58:61] cbsz:4 blgp:4
	v_mfma_f32_16x16x128_f8f6f4 v[66:69], v[212:215], v[196:199], v[66:69] cbsz:4 blgp:4
	v_mfma_f32_16x16x128_f8f6f4 v[66:69], v[220:223], v[204:207], v[66:69] cbsz:4 blgp:4
	v_mfma_f32_16x16x128_f8f6f4 v[74:77], v[212:215], v[200:203], v[74:77] cbsz:4 blgp:4
	v_mfma_f32_16x16x128_f8f6f4 v[74:77], v[220:223], v[208:211], v[74:77] cbsz:4 blgp:4
	v_mfma_f32_16x16x128_f8f6f4 v[54:57], v[216:219], v[180:183], v[54:57] cbsz:4 blgp:4
	v_mfma_f32_16x16x128_f8f6f4 v[54:57], v[224:227], v[188:191], v[54:57] cbsz:4 blgp:4
	v_mfma_f32_16x16x128_f8f6f4 v[62:65], v[216:219], v[184:187], v[62:65] cbsz:4 blgp:4
	v_mfma_f32_16x16x128_f8f6f4 v[62:65], v[224:227], v[192:195], v[62:65] cbsz:4 blgp:4
	v_mfma_f32_16x16x128_f8f6f4 v[70:73], v[216:219], v[196:199], v[70:73] cbsz:4 blgp:4
	v_mfma_f32_16x16x128_f8f6f4 v[70:73], v[224:227], v[204:207], v[70:73] cbsz:4 blgp:4
	v_mfma_f32_16x16x128_f8f6f4 v[78:81], v[216:219], v[200:203], v[78:81] cbsz:4 blgp:4
	v_mfma_f32_16x16x128_f8f6f4 v[78:81], v[224:227], v[208:211], v[78:81] cbsz:4 blgp:4
	s_setprio 0
	s_barrier
	s_mov_b32 m0, s65
	s_nop 0
	global_load_lds_dwordx4 v148, s[44:45]
	s_mov_b32 m0, s66
	s_nop 0
	global_load_lds_dwordx4 v152, s[44:45]
	ds_read_b128 v[180:183], v165 offset:49152
	ds_read_b128 v[184:187], v165 offset:51200
	ds_read_b128 v[188:191], v166 offset:49152
	ds_read_b128 v[192:195], v166 offset:51200
	ds_read_b128 v[196:199], v165 offset:53248
	ds_read_b128 v[200:203], v165 offset:55296
	ds_read_b128 v[204:207], v166 offset:53248
	ds_read_b128 v[208:211], v166 offset:55296
	s_mov_b32 m0, s67
	s_nop 0
	global_load_lds_dwordx4 v146, s[46:47]
	s_mov_b32 m0, s68
	s_nop 0
	global_load_lds_dwordx4 v150, s[46:47]
	s_add_u32 s44, s44, s24
	s_addc_u32 s45, s45, s25
	s_mov_b32 m0, s69
	s_nop 0
	global_load_lds_dwordx4 v148, s[44:45]
	s_mov_b32 m0, s70
	s_nop 0
	global_load_lds_dwordx4 v152, s[44:45]
	s_waitcnt vmcnt(8)
	s_waitcnt lgkmcnt(0)
	s_barrier
	s_setprio 1
	v_mfma_f32_16x16x128_f8f6f4 v[86:89], v[156:159], v[180:183], v[86:89] cbsz:4 blgp:4
	v_mfma_f32_16x16x128_f8f6f4 v[86:89], v[172:175], v[188:191], v[86:89] cbsz:4 blgp:4
	v_mfma_f32_16x16x128_f8f6f4 v[98:101], v[156:159], v[184:187], v[98:101] cbsz:4 blgp:4
	v_mfma_f32_16x16x128_f8f6f4 v[98:101], v[172:175], v[192:195], v[98:101] cbsz:4 blgp:4
	v_mfma_f32_16x16x128_f8f6f4 v[118:121], v[156:159], v[196:199], v[118:121] cbsz:4 blgp:4
	v_mfma_f32_16x16x128_f8f6f4 v[118:121], v[172:175], v[204:207], v[118:121] cbsz:4 blgp:4
	v_mfma_f32_16x16x128_f8f6f4 v[138:141], v[156:159], v[200:203], v[138:141] cbsz:4 blgp:4
	v_mfma_f32_16x16x128_f8f6f4 v[138:141], v[172:175], v[208:211], v[138:141] cbsz:4 blgp:4
	v_mfma_f32_16x16x128_f8f6f4 v[90:93], v[168:171], v[180:183], v[90:93] cbsz:4 blgp:4
	v_mfma_f32_16x16x128_f8f6f4 v[90:93], v[176:179], v[188:191], v[90:93] cbsz:4 blgp:4
	v_mfma_f32_16x16x128_f8f6f4 v[106:109], v[168:171], v[184:187], v[106:109] cbsz:4 blgp:4
	v_mfma_f32_16x16x128_f8f6f4 v[106:109], v[176:179], v[192:195], v[106:109] cbsz:4 blgp:4
	v_mfma_f32_16x16x128_f8f6f4 v[126:129], v[168:171], v[196:199], v[126:129] cbsz:4 blgp:4
	v_mfma_f32_16x16x128_f8f6f4 v[126:129], v[176:179], v[204:207], v[126:129] cbsz:4 blgp:4
	v_mfma_f32_16x16x128_f8f6f4 v[82:85], v[168:171], v[200:203], v[82:85] cbsz:4 blgp:4
	v_mfma_f32_16x16x128_f8f6f4 v[82:85], v[176:179], v[208:211], v[82:85] cbsz:4 blgp:4
	v_mfma_f32_16x16x128_f8f6f4 v[94:97], v[212:215], v[180:183], v[94:97] cbsz:4 blgp:4
	v_mfma_f32_16x16x128_f8f6f4 v[94:97], v[220:223], v[188:191], v[94:97] cbsz:4 blgp:4
	v_mfma_f32_16x16x128_f8f6f4 v[110:113], v[212:215], v[184:187], v[110:113] cbsz:4 blgp:4
	v_mfma_f32_16x16x128_f8f6f4 v[110:113], v[220:223], v[192:195], v[110:113] cbsz:4 blgp:4
	v_mfma_f32_16x16x128_f8f6f4 v[122:125], v[212:215], v[196:199], v[122:125] cbsz:4 blgp:4
	v_mfma_f32_16x16x128_f8f6f4 v[122:125], v[220:223], v[204:207], v[122:125] cbsz:4 blgp:4
	v_mfma_f32_16x16x128_f8f6f4 v[134:137], v[212:215], v[200:203], v[134:137] cbsz:4 blgp:4
	v_mfma_f32_16x16x128_f8f6f4 v[134:137], v[220:223], v[208:211], v[134:137] cbsz:4 blgp:4
	v_mfma_f32_16x16x128_f8f6f4 v[102:105], v[216:219], v[180:183], v[102:105] cbsz:4 blgp:4
	v_mfma_f32_16x16x128_f8f6f4 v[102:105], v[224:227], v[188:191], v[102:105] cbsz:4 blgp:4
	v_mfma_f32_16x16x128_f8f6f4 v[114:117], v[216:219], v[184:187], v[114:117] cbsz:4 blgp:4
	v_mfma_f32_16x16x128_f8f6f4 v[114:117], v[224:227], v[192:195], v[114:117] cbsz:4 blgp:4
	v_mfma_f32_16x16x128_f8f6f4 v[130:133], v[216:219], v[196:199], v[130:133] cbsz:4 blgp:4
	v_mfma_f32_16x16x128_f8f6f4 v[130:133], v[224:227], v[204:207], v[130:133] cbsz:4 blgp:4
	v_mfma_f32_16x16x128_f8f6f4 v[142:145], v[216:219], v[200:203], v[142:145] cbsz:4 blgp:4
	v_mfma_f32_16x16x128_f8f6f4 v[142:145], v[224:227], v[208:211], v[142:145] cbsz:4 blgp:4
	s_setprio 0
	s_andn2_b64 vcc, exec, s[34:35]
	s_barrier
	s_cbranch_vccnz .LBB5_4
	s_ashr_i32 s29, s28, 31
	s_lshl_b64 s[44:45], s[28:29], 10
	s_add_u32 s44, s10, s44
	s_addc_u32 s45, s11, s45
	s_add_u32 s29, s42, 0x200
	s_addc_u32 s79, s43, 0
	s_add_u32 s80, s40, 0x200
	s_addc_u32 s81, s41, 0
	s_add_u32 s40, s82, 0x180
	s_addc_u32 s41, s83, 0
	s_mov_b32 s82, 4
	s_cmp_eq_u32 s64, s82
	s_cselect_b64 s[42:43], -1, 0
	s_cmp_lg_u32 s64, s82
	s_cbranch_scc1 .LBB5_15

.LBB5_15:
	ds_read_b128 v[156:159], v163
	ds_read_b128 v[168:171], v163 offset:2048
	ds_read_b128 v[172:175], v164
	ds_read_b128 v[176:179], v164 offset:2048
	s_and_b64 s[42:43], s[42:43], exec
	s_cselect_b32 s48, s38, s29
	s_cselect_b32 s49, s39, s79
	s_cselect_b32 s51, s5, s81
	s_cselect_b32 s50, s4, s80
	s_add_u32 s46, s48, 0x80
	s_addc_u32 s47, s49, 0
	s_add_u32 s42, s50, 0x80
	s_addc_u32 s43, s51, 0
	ds_read_b128 v[180:183], v165
	ds_read_b128 v[184:187], v165 offset:2048
	ds_read_b128 v[188:191], v166
	ds_read_b128 v[192:195], v166 offset:2048
	ds_read_b128 v[196:199], v165 offset:4096
	ds_read_b128 v[200:203], v165 offset:6144
	ds_read_b128 v[204:207], v166 offset:4096
	ds_read_b128 v[208:211], v166 offset:6144
	s_mov_b32 m0, s71
	s_nop 0
	global_load_lds_dwordx4 v146, s[40:41]
	s_mov_b32 m0, s72
	s_nop 0
	global_load_lds_dwordx4 v150, s[40:41]
	s_waitcnt lgkmcnt(8)
	ds_read_b128 v[212:215], v163 offset:16384
	ds_read_b128 v[216:219], v163 offset:18432
	ds_read_b128 v[220:223], v164 offset:16384
	ds_read_b128 v[224:227], v164 offset:18432
	s_waitcnt vmcnt(8)
	s_waitcnt lgkmcnt(0)
	s_barrier
	s_waitcnt lgkmcnt(0)
	s_setprio 1
	v_mfma_f32_16x16x128_f8f6f4 v[18:21], v[156:159], v[180:183], v[18:21] cbsz:4 blgp:4
	v_mfma_f32_16x16x128_f8f6f4 v[18:21], v[172:175], v[188:191], v[18:21] cbsz:4 blgp:4
	v_mfma_f32_16x16x128_f8f6f4 v[26:29], v[156:159], v[184:187], v[26:29] cbsz:4 blgp:4
	v_mfma_f32_16x16x128_f8f6f4 v[26:29], v[172:175], v[192:195], v[26:29] cbsz:4 blgp:4
	v_mfma_f32_16x16x128_f8f6f4 v[34:37], v[156:159], v[196:199], v[34:37] cbsz:4 blgp:4
	v_mfma_f32_16x16x128_f8f6f4 v[34:37], v[172:175], v[204:207], v[34:37] cbsz:4 blgp:4
	v_mfma_f32_16x16x128_f8f6f4 v[42:45], v[156:159], v[200:203], v[42:45] cbsz:4 blgp:4
	v_mfma_f32_16x16x128_f8f6f4 v[42:45], v[172:175], v[208:211], v[42:45] cbsz:4 blgp:4
	v_mfma_f32_16x16x128_f8f6f4 v[22:25], v[168:171], v[180:183], v[22:25] cbsz:4 blgp:4
	v_mfma_f32_16x16x128_f8f6f4 v[22:25], v[176:179], v[188:191], v[22:25] cbsz:4 blgp:4
	v_mfma_f32_16x16x128_f8f6f4 v[30:33], v[168:171], v[184:187], v[30:33] cbsz:4 blgp:4
	v_mfma_f32_16x16x128_f8f6f4 v[30:33], v[176:179], v[192:195], v[30:33] cbsz:4 blgp:4
	v_mfma_f32_16x16x128_f8f6f4 v[38:41], v[168:171], v[196:199], v[38:41] cbsz:4 blgp:4
	v_mfma_f32_16x16x128_f8f6f4 v[38:41], v[176:179], v[204:207], v[38:41] cbsz:4 blgp:4
	v_mfma_f32_16x16x128_f8f6f4 v[46:49], v[168:171], v[200:203], v[46:49] cbsz:4 blgp:4
	v_mfma_f32_16x16x128_f8f6f4 v[46:49], v[176:179], v[208:211], v[46:49] cbsz:4 blgp:4
	v_mfma_f32_16x16x128_f8f6f4 v[50:53], v[212:215], v[180:183], v[50:53] cbsz:4 blgp:4
	v_mfma_f32_16x16x128_f8f6f4 v[50:53], v[220:223], v[188:191], v[50:53] cbsz:4 blgp:4
	v_mfma_f32_16x16x128_f8f6f4 v[58:61], v[212:215], v[184:187], v[58:61] cbsz:4 blgp:4
	v_mfma_f32_16x16x128_f8f6f4 v[58:61], v[220:223], v[192:195], v[58:61] cbsz:4 blgp:4
	v_mfma_f32_16x16x128_f8f6f4 v[66:69], v[212:215], v[196:199], v[66:69] cbsz:4 blgp:4
	v_mfma_f32_16x16x128_f8f6f4 v[66:69], v[220:223], v[204:207], v[66:69] cbsz:4 blgp:4
	v_mfma_f32_16x16x128_f8f6f4 v[74:77], v[212:215], v[200:203], v[74:77] cbsz:4 blgp:4
	v_mfma_f32_16x16x128_f8f6f4 v[74:77], v[220:223], v[208:211], v[74:77] cbsz:4 blgp:4
	v_mfma_f32_16x16x128_f8f6f4 v[54:57], v[216:219], v[180:183], v[54:57] cbsz:4 blgp:4
	v_mfma_f32_16x16x128_f8f6f4 v[54:57], v[224:227], v[188:191], v[54:57] cbsz:4 blgp:4
	v_mfma_f32_16x16x128_f8f6f4 v[62:65], v[216:219], v[184:187], v[62:65] cbsz:4 blgp:4
	v_mfma_f32_16x16x128_f8f6f4 v[62:65], v[224:227], v[192:195], v[62:65] cbsz:4 blgp:4
	v_mfma_f32_16x16x128_f8f6f4 v[70:73], v[216:219], v[196:199], v[70:73] cbsz:4 blgp:4
	v_mfma_f32_16x16x128_f8f6f4 v[70:73], v[224:227], v[204:207], v[70:73] cbsz:4 blgp:4
	v_mfma_f32_16x16x128_f8f6f4 v[78:81], v[216:219], v[200:203], v[78:81] cbsz:4 blgp:4
	v_mfma_f32_16x16x128_f8f6f4 v[78:81], v[224:227], v[208:211], v[78:81] cbsz:4 blgp:4
	s_setprio 0
	s_barrier
	s_mov_b32 m0, s56
	s_nop 0
	global_load_lds_dwordx4 v148, s[50:51]
	s_mov_b32 m0, s57
	s_nop 0
	global_load_lds_dwordx4 v152, s[50:51]
	ds_read_b128 v[180:183], v165 offset:16384
	ds_read_b128 v[184:187], v165 offset:18432
	ds_read_b128 v[188:191], v166 offset:16384
	ds_read_b128 v[192:195], v166 offset:18432
	ds_read_b128 v[196:199], v165 offset:20480
	ds_read_b128 v[200:203], v165 offset:22528
	ds_read_b128 v[204:207], v166 offset:20480
	ds_read_b128 v[208:211], v166 offset:22528
	s_mov_b32 m0, s55
	s_nop 0
	global_load_lds_dwordx4 v146, s[48:49]
	s_mov_b32 m0, s58
	s_nop 0
	global_load_lds_dwordx4 v150, s[48:49]
	s_add_u32 s50, s50, s24
	s_addc_u32 s51, s51, s25
	s_mov_b32 m0, s59
	s_nop 0
	global_load_lds_dwordx4 v148, s[50:51]
	s_mov_b32 m0, s60
	s_nop 0
	global_load_lds_dwordx4 v152, s[50:51]
	s_waitcnt vmcnt(8)
	s_waitcnt lgkmcnt(0)
	s_barrier
	s_setprio 1
	v_mfma_f32_16x16x128_f8f6f4 v[86:89], v[156:159], v[180:183], v[86:89] cbsz:4 blgp:4
	v_mfma_f32_16x16x128_f8f6f4 v[86:89], v[172:175], v[188:191], v[86:89] cbsz:4 blgp:4
	v_mfma_f32_16x16x128_f8f6f4 v[98:101], v[156:159], v[184:187], v[98:101] cbsz:4 blgp:4
	v_mfma_f32_16x16x128_f8f6f4 v[98:101], v[172:175], v[192:195], v[98:101] cbsz:4 blgp:4
	v_mfma_f32_16x16x128_f8f6f4 v[118:121], v[156:159], v[196:199], v[118:121] cbsz:4 blgp:4
	v_mfma_f32_16x16x128_f8f6f4 v[118:121], v[172:175], v[204:207], v[118:121] cbsz:4 blgp:4
	v_mfma_f32_16x16x128_f8f6f4 v[138:141], v[156:159], v[200:203], v[138:141] cbsz:4 blgp:4
	v_mfma_f32_16x16x128_f8f6f4 v[138:141], v[172:175], v[208:211], v[138:141] cbsz:4 blgp:4
	v_mfma_f32_16x16x128_f8f6f4 v[90:93], v[168:171], v[180:183], v[90:93] cbsz:4 blgp:4
	v_mfma_f32_16x16x128_f8f6f4 v[90:93], v[176:179], v[188:191], v[90:93] cbsz:4 blgp:4
	v_mfma_f32_16x16x128_f8f6f4 v[106:109], v[168:171], v[184:187], v[106:109] cbsz:4 blgp:4
	v_mfma_f32_16x16x128_f8f6f4 v[106:109], v[176:179], v[192:195], v[106:109] cbsz:4 blgp:4
	v_mfma_f32_16x16x128_f8f6f4 v[126:129], v[168:171], v[196:199], v[126:129] cbsz:4 blgp:4
	v_mfma_f32_16x16x128_f8f6f4 v[126:129], v[176:179], v[204:207], v[126:129] cbsz:4 blgp:4
	v_mfma_f32_16x16x128_f8f6f4 v[82:85], v[168:171], v[200:203], v[82:85] cbsz:4 blgp:4
	v_mfma_f32_16x16x128_f8f6f4 v[82:85], v[176:179], v[208:211], v[82:85] cbsz:4 blgp:4
	v_mfma_f32_16x16x128_f8f6f4 v[94:97], v[212:215], v[180:183], v[94:97] cbsz:4 blgp:4
	v_mfma_f32_16x16x128_f8f6f4 v[94:97], v[220:223], v[188:191], v[94:97] cbsz:4 blgp:4
	v_mfma_f32_16x16x128_f8f6f4 v[110:113], v[212:215], v[184:187], v[110:113] cbsz:4 blgp:4
	v_mfma_f32_16x16x128_f8f6f4 v[110:113], v[220:223], v[192:195], v[110:113] cbsz:4 blgp:4
	v_mfma_f32_16x16x128_f8f6f4 v[122:125], v[212:215], v[196:199], v[122:125] cbsz:4 blgp:4
	v_mfma_f32_16x16x128_f8f6f4 v[122:125], v[220:223], v[204:207], v[122:125] cbsz:4 blgp:4
	v_mfma_f32_16x16x128_f8f6f4 v[134:137], v[212:215], v[200:203], v[134:137] cbsz:4 blgp:4
	v_mfma_f32_16x16x128_f8f6f4 v[134:137], v[220:223], v[208:211], v[134:137] cbsz:4 blgp:4
	v_mfma_f32_16x16x128_f8f6f4 v[102:105], v[216:219], v[180:183], v[102:105] cbsz:4 blgp:4
	v_mfma_f32_16x16x128_f8f6f4 v[102:105], v[224:227], v[188:191], v[102:105] cbsz:4 blgp:4
	v_mfma_f32_16x16x128_f8f6f4 v[114:117], v[216:219], v[184:187], v[114:117] cbsz:4 blgp:4
	v_mfma_f32_16x16x128_f8f6f4 v[114:117], v[224:227], v[192:195], v[114:117] cbsz:4 blgp:4
	v_mfma_f32_16x16x128_f8f6f4 v[130:133], v[216:219], v[196:199], v[130:133] cbsz:4 blgp:4
	v_mfma_f32_16x16x128_f8f6f4 v[130:133], v[224:227], v[204:207], v[130:133] cbsz:4 blgp:4
	v_mfma_f32_16x16x128_f8f6f4 v[142:145], v[216:219], v[200:203], v[142:145] cbsz:4 blgp:4
	v_mfma_f32_16x16x128_f8f6f4 v[142:145], v[224:227], v[208:211], v[142:145] cbsz:4 blgp:4
	s_setprio 0
	s_barrier
	ds_read_b128 v[156:159], v163 offset:32768
	ds_read_b128 v[168:171], v163 offset:34816
	ds_read_b128 v[172:175], v164 offset:32768
	ds_read_b128 v[176:179], v164 offset:34816
	ds_read_b128 v[180:183], v165 offset:32768
	ds_read_b128 v[184:187], v165 offset:34816
	ds_read_b128 v[188:191], v166 offset:32768
	ds_read_b128 v[192:195], v166 offset:34816
	ds_read_b128 v[196:199], v165 offset:36864
	ds_read_b128 v[200:203], v165 offset:38912
	ds_read_b128 v[204:207], v166 offset:36864
	ds_read_b128 v[208:211], v166 offset:38912
	s_add_u32 s48, s48, s22
	s_addc_u32 s49, s49, s23
	s_mov_b32 m0, s61
	s_nop 0
	global_load_lds_dwordx4 v146, s[48:49]
	s_mov_b32 m0, s62
	s_nop 0
	global_load_lds_dwordx4 v150, s[48:49]
	s_waitcnt lgkmcnt(8)
	ds_read_b128 v[212:215], v163 offset:49152
	ds_read_b128 v[216:219], v163 offset:51200
	ds_read_b128 v[220:223], v164 offset:49152
	ds_read_b128 v[224:227], v164 offset:51200
	s_waitcnt vmcnt(8)
	s_waitcnt lgkmcnt(0)
	s_barrier
	s_waitcnt lgkmcnt(0)
	s_setprio 1
	v_mfma_f32_16x16x128_f8f6f4 v[18:21], v[156:159], v[180:183], v[18:21] cbsz:4 blgp:4
	v_mfma_f32_16x16x128_f8f6f4 v[18:21], v[172:175], v[188:191], v[18:21] cbsz:4 blgp:4
	v_mfma_f32_16x16x128_f8f6f4 v[26:29], v[156:159], v[184:187], v[26:29] cbsz:4 blgp:4
	v_mfma_f32_16x16x128_f8f6f4 v[26:29], v[172:175], v[192:195], v[26:29] cbsz:4 blgp:4
	v_mfma_f32_16x16x128_f8f6f4 v[34:37], v[156:159], v[196:199], v[34:37] cbsz:4 blgp:4
	v_mfma_f32_16x16x128_f8f6f4 v[34:37], v[172:175], v[204:207], v[34:37] cbsz:4 blgp:4
	v_mfma_f32_16x16x128_f8f6f4 v[42:45], v[156:159], v[200:203], v[42:45] cbsz:4 blgp:4
	v_mfma_f32_16x16x128_f8f6f4 v[42:45], v[172:175], v[208:211], v[42:45] cbsz:4 blgp:4
	v_mfma_f32_16x16x128_f8f6f4 v[22:25], v[168:171], v[180:183], v[22:25] cbsz:4 blgp:4
	v_mfma_f32_16x16x128_f8f6f4 v[22:25], v[176:179], v[188:191], v[22:25] cbsz:4 blgp:4
	v_mfma_f32_16x16x128_f8f6f4 v[30:33], v[168:171], v[184:187], v[30:33] cbsz:4 blgp:4
	v_mfma_f32_16x16x128_f8f6f4 v[30:33], v[176:179], v[192:195], v[30:33] cbsz:4 blgp:4
	v_mfma_f32_16x16x128_f8f6f4 v[38:41], v[168:171], v[196:199], v[38:41] cbsz:4 blgp:4
	v_mfma_f32_16x16x128_f8f6f4 v[38:41], v[176:179], v[204:207], v[38:41] cbsz:4 blgp:4
	v_mfma_f32_16x16x128_f8f6f4 v[46:49], v[168:171], v[200:203], v[46:49] cbsz:4 blgp:4
	v_mfma_f32_16x16x128_f8f6f4 v[46:49], v[176:179], v[208:211], v[46:49] cbsz:4 blgp:4
	v_mfma_f32_16x16x128_f8f6f4 v[50:53], v[212:215], v[180:183], v[50:53] cbsz:4 blgp:4
	v_mfma_f32_16x16x128_f8f6f4 v[50:53], v[220:223], v[188:191], v[50:53] cbsz:4 blgp:4
	v_mfma_f32_16x16x128_f8f6f4 v[58:61], v[212:215], v[184:187], v[58:61] cbsz:4 blgp:4
	v_mfma_f32_16x16x128_f8f6f4 v[58:61], v[220:223], v[192:195], v[58:61] cbsz:4 blgp:4
	v_mfma_f32_16x16x128_f8f6f4 v[66:69], v[212:215], v[196:199], v[66:69] cbsz:4 blgp:4
	v_mfma_f32_16x16x128_f8f6f4 v[66:69], v[220:223], v[204:207], v[66:69] cbsz:4 blgp:4
	v_mfma_f32_16x16x128_f8f6f4 v[74:77], v[212:215], v[200:203], v[74:77] cbsz:4 blgp:4
	v_mfma_f32_16x16x128_f8f6f4 v[74:77], v[220:223], v[208:211], v[74:77] cbsz:4 blgp:4
	v_mfma_f32_16x16x128_f8f6f4 v[54:57], v[216:219], v[180:183], v[54:57] cbsz:4 blgp:4
	v_mfma_f32_16x16x128_f8f6f4 v[54:57], v[224:227], v[188:191], v[54:57] cbsz:4 blgp:4
	v_mfma_f32_16x16x128_f8f6f4 v[62:65], v[216:219], v[184:187], v[62:65] cbsz:4 blgp:4
	v_mfma_f32_16x16x128_f8f6f4 v[62:65], v[224:227], v[192:195], v[62:65] cbsz:4 blgp:4
	v_mfma_f32_16x16x128_f8f6f4 v[70:73], v[216:219], v[196:199], v[70:73] cbsz:4 blgp:4
	v_mfma_f32_16x16x128_f8f6f4 v[70:73], v[224:227], v[204:207], v[70:73] cbsz:4 blgp:4
	v_mfma_f32_16x16x128_f8f6f4 v[78:81], v[216:219], v[200:203], v[78:81] cbsz:4 blgp:4
	v_mfma_f32_16x16x128_f8f6f4 v[78:81], v[224:227], v[208:211], v[78:81] cbsz:4 blgp:4
	s_setprio 0
	s_barrier
	s_mov_b32 m0, s65
	s_nop 0
	global_load_lds_dwordx4 v148, s[42:43]
	s_mov_b32 m0, s66
	s_nop 0
	global_load_lds_dwordx4 v152, s[42:43]
	ds_read_b128 v[180:183], v165 offset:49152
	ds_read_b128 v[184:187], v165 offset:51200
	ds_read_b128 v[188:191], v166 offset:49152
	ds_read_b128 v[192:195], v166 offset:51200
	ds_read_b128 v[196:199], v165 offset:53248
	ds_read_b128 v[200:203], v165 offset:55296
	ds_read_b128 v[204:207], v166 offset:53248
	ds_read_b128 v[208:211], v166 offset:55296
	s_mov_b32 m0, s67
	s_nop 0
	global_load_lds_dwordx4 v146, s[46:47]
	s_mov_b32 m0, s68
	s_nop 0
	global_load_lds_dwordx4 v150, s[46:47]
	s_add_u32 s42, s42, s24
	s_addc_u32 s43, s43, s25
	s_mov_b32 m0, s69
	s_nop 0
	global_load_lds_dwordx4 v148, s[42:43]
	s_mov_b32 m0, s70
	s_nop 0
	global_load_lds_dwordx4 v152, s[42:43]
	s_waitcnt vmcnt(8)
	s_waitcnt lgkmcnt(0)
	s_barrier
	s_setprio 1
	v_mfma_f32_16x16x128_f8f6f4 v[86:89], v[156:159], v[180:183], v[86:89] cbsz:4 blgp:4
	v_mfma_f32_16x16x128_f8f6f4 v[86:89], v[172:175], v[188:191], v[86:89] cbsz:4 blgp:4
	v_mfma_f32_16x16x128_f8f6f4 v[98:101], v[156:159], v[184:187], v[98:101] cbsz:4 blgp:4
	v_mfma_f32_16x16x128_f8f6f4 v[98:101], v[172:175], v[192:195], v[98:101] cbsz:4 blgp:4
	v_mfma_f32_16x16x128_f8f6f4 v[118:121], v[156:159], v[196:199], v[118:121] cbsz:4 blgp:4
	v_mfma_f32_16x16x128_f8f6f4 v[118:121], v[172:175], v[204:207], v[118:121] cbsz:4 blgp:4
	v_mfma_f32_16x16x128_f8f6f4 v[138:141], v[156:159], v[200:203], v[138:141] cbsz:4 blgp:4
	v_mfma_f32_16x16x128_f8f6f4 v[138:141], v[172:175], v[208:211], v[138:141] cbsz:4 blgp:4
	v_mfma_f32_16x16x128_f8f6f4 v[90:93], v[168:171], v[180:183], v[90:93] cbsz:4 blgp:4
	v_mfma_f32_16x16x128_f8f6f4 v[90:93], v[176:179], v[188:191], v[90:93] cbsz:4 blgp:4
	v_mfma_f32_16x16x128_f8f6f4 v[106:109], v[168:171], v[184:187], v[106:109] cbsz:4 blgp:4
	v_mfma_f32_16x16x128_f8f6f4 v[106:109], v[176:179], v[192:195], v[106:109] cbsz:4 blgp:4
	v_mfma_f32_16x16x128_f8f6f4 v[126:129], v[168:171], v[196:199], v[126:129] cbsz:4 blgp:4
	v_mfma_f32_16x16x128_f8f6f4 v[126:129], v[176:179], v[204:207], v[126:129] cbsz:4 blgp:4
	v_mfma_f32_16x16x128_f8f6f4 v[82:85], v[168:171], v[200:203], v[82:85] cbsz:4 blgp:4
	v_mfma_f32_16x16x128_f8f6f4 v[82:85], v[176:179], v[208:211], v[82:85] cbsz:4 blgp:4
	v_mfma_f32_16x16x128_f8f6f4 v[94:97], v[212:215], v[180:183], v[94:97] cbsz:4 blgp:4
	v_mfma_f32_16x16x128_f8f6f4 v[94:97], v[220:223], v[188:191], v[94:97] cbsz:4 blgp:4
	v_mfma_f32_16x16x128_f8f6f4 v[110:113], v[212:215], v[184:187], v[110:113] cbsz:4 blgp:4
	v_mfma_f32_16x16x128_f8f6f4 v[110:113], v[220:223], v[192:195], v[110:113] cbsz:4 blgp:4
	v_mfma_f32_16x16x128_f8f6f4 v[122:125], v[212:215], v[196:199], v[122:125] cbsz:4 blgp:4
	v_mfma_f32_16x16x128_f8f6f4 v[122:125], v[220:223], v[204:207], v[122:125] cbsz:4 blgp:4
	v_mfma_f32_16x16x128_f8f6f4 v[134:137], v[212:215], v[200:203], v[134:137] cbsz:4 blgp:4
	v_mfma_f32_16x16x128_f8f6f4 v[134:137], v[220:223], v[208:211], v[134:137] cbsz:4 blgp:4
	v_mfma_f32_16x16x128_f8f6f4 v[102:105], v[216:219], v[180:183], v[102:105] cbsz:4 blgp:4
	v_mfma_f32_16x16x128_f8f6f4 v[102:105], v[224:227], v[188:191], v[102:105] cbsz:4 blgp:4
	v_mfma_f32_16x16x128_f8f6f4 v[114:117], v[216:219], v[184:187], v[114:117] cbsz:4 blgp:4
	v_mfma_f32_16x16x128_f8f6f4 v[114:117], v[224:227], v[192:195], v[114:117] cbsz:4 blgp:4
	v_mfma_f32_16x16x128_f8f6f4 v[130:133], v[216:219], v[196:199], v[130:133] cbsz:4 blgp:4
	v_mfma_f32_16x16x128_f8f6f4 v[130:133], v[224:227], v[204:207], v[130:133] cbsz:4 blgp:4
	v_mfma_f32_16x16x128_f8f6f4 v[142:145], v[216:219], v[200:203], v[142:145] cbsz:4 blgp:4
	v_mfma_f32_16x16x128_f8f6f4 v[142:145], v[224:227], v[208:211], v[142:145] cbsz:4 blgp:4
	s_setprio 0
	s_add_i32 s42, s82, 2
	s_add_u32 s29, s29, 0x100
	s_addc_u32 s79, s79, 0
	s_add_u32 s80, s80, 0x100
	s_addc_u32 s81, s81, 0
	s_add_u32 s40, s40, 0x100
	s_addc_u32 s41, s41, 0
	s_cmp_ge_i32 s82, s64
	s_barrier
	s_cbranch_scc1 .LBB5_4
	s_mov_b32 s82, s42
	s_cmp_eq_u32 s64, s82
	s_cselect_b64 s[42:43], -1, 0
	s_cmp_lg_u32 s64, s82
	s_cbranch_scc0 .LBB5_14
	s_branch .LBB5_15

.LBB6_15:
	s_add_u32 s82, s36, s20
	s_addc_u32 s83, s37, s21
	s_add_u32 s31, s36, 0x100
	s_addc_u32 s39, s37, 0
	s_and_b64 s[40:41], s[12:13], exec
	ds_read_b128 v[82:85], v169
	ds_read_b128 v[94:97], v169 offset:2048
	ds_read_b128 v[102:105], v178
	ds_read_b128 v[110:113], v178 offset:2048
	s_cselect_b32 s45, s5, s39
	s_cselect_b32 s44, s4, s31
	s_add_u32 s31, s34, 0x100
	s_addc_u32 s39, s35, 0
	s_and_b64 s[40:41], s[12:13], exec
	s_cselect_b32 s47, s7, s39
	s_cselect_b32 s46, s6, s31
	s_add_u32 s42, s44, 0x80
	s_addc_u32 s43, s45, 0
	s_add_u32 s40, s46, 0x80
	s_addc_u32 s41, s47, 0
	ds_read_b128 v[58:61], v179
	ds_read_b128 v[66:69], v179 offset:2048
	ds_read_b128 v[62:65], v180
	ds_read_b128 v[70:73], v180 offset:2048
	ds_read_b128 v[74:77], v179 offset:4096
	ds_read_b128 v[86:89], v179 offset:6144
	ds_read_b128 v[78:81], v180 offset:4096
	ds_read_b128 v[90:93], v180 offset:6144
	s_add_u32 s84, s82, 0x80
	s_addc_u32 s85, s83, 0
	s_mov_b32 m0, s68
	s_nop 0
	global_load_lds_dwordx4 v162, s[84:85]
	s_mov_b32 m0, s69
	s_nop 0
	global_load_lds_dwordx4 v166, s[84:85]
	s_waitcnt lgkmcnt(8)
	ds_read_b128 v[142:145], v169 offset:16384
	ds_read_b128 v[146:149], v169 offset:18432
	ds_read_b128 v[150:153], v178 offset:16384
	ds_read_b128 v[154:157], v178 offset:18432
	s_waitcnt vmcnt(8)
	s_waitcnt lgkmcnt(0)
	s_barrier
	s_waitcnt lgkmcnt(0)
	s_waitcnt vmcnt(16)
	v_mov_b32_e32 v171, v170
	v_pk_mul_f32 v[16:17], v[170:171], v[16:17]
	v_pk_mul_f32 v[14:15], v[172:173], v[14:15]
	v_pk_mul_f32 v[12:13], v[170:171], v[12:13]
	v_pk_mul_f32 v[10:11], v[172:173], v[10:11]
	v_pk_mul_f32 v[8:9], v[170:171], v[8:9]
	v_pk_mul_f32 v[6:7], v[172:173], v[6:7]
	v_pk_mul_f32 v[4:5], v[170:171], v[4:5]
	v_pk_mul_f32 v[2:3], v[172:173], v[2:3]
	s_setprio 1
	v_mfma_f32_16x16x128_f8f6f4 v[18:21], v[82:85], v[58:61], v[14:17] cbsz:4 blgp:4
	v_mfma_f32_16x16x128_f8f6f4 v[18:21], v[102:105], v[62:65], v[18:21] cbsz:4 blgp:4
	v_mfma_f32_16x16x128_f8f6f4 v[26:29], v[82:85], v[66:69], v[14:17] cbsz:4 blgp:4
	v_mfma_f32_16x16x128_f8f6f4 v[26:29], v[102:105], v[70:73], v[26:29] cbsz:4 blgp:4
	v_mfma_f32_16x16x128_f8f6f4 v[34:37], v[82:85], v[74:77], v[14:17] cbsz:4 blgp:4
	v_mfma_f32_16x16x128_f8f6f4 v[34:37], v[102:105], v[78:81], v[34:37] cbsz:4 blgp:4
	v_mfma_f32_16x16x128_f8f6f4 v[42:45], v[82:85], v[86:89], v[14:17] cbsz:4 blgp:4
	v_mfma_f32_16x16x128_f8f6f4 v[42:45], v[102:105], v[90:93], v[42:45] cbsz:4 blgp:4
	v_mfma_f32_16x16x128_f8f6f4 v[22:25], v[94:97], v[58:61], v[10:13] cbsz:4 blgp:4
	v_mfma_f32_16x16x128_f8f6f4 v[22:25], v[110:113], v[62:65], v[22:25] cbsz:4 blgp:4
	v_mfma_f32_16x16x128_f8f6f4 v[30:33], v[94:97], v[66:69], v[10:13] cbsz:4 blgp:4
	v_mfma_f32_16x16x128_f8f6f4 v[30:33], v[110:113], v[70:73], v[30:33] cbsz:4 blgp:4
	v_mfma_f32_16x16x128_f8f6f4 v[38:41], v[94:97], v[74:77], v[10:13] cbsz:4 blgp:4
	v_mfma_f32_16x16x128_f8f6f4 v[38:41], v[110:113], v[78:81], v[38:41] cbsz:4 blgp:4
	v_mfma_f32_16x16x128_f8f6f4 v[46:49], v[94:97], v[86:89], v[10:13] cbsz:4 blgp:4
	v_mfma_f32_16x16x128_f8f6f4 v[46:49], v[110:113], v[90:93], v[46:49] cbsz:4 blgp:4
	v_mfma_f32_16x16x128_f8f6f4 v[50:53], v[142:145], v[58:61], v[6:9] cbsz:4 blgp:4
	v_mfma_f32_16x16x128_f8f6f4 v[50:53], v[150:153], v[62:65], v[50:53] cbsz:4 blgp:4
	v_mfma_f32_16x16x128_f8f6f4 v[54:57], v[146:149], v[58:61], v[2:5] cbsz:4 blgp:4
	v_mfma_f32_16x16x128_f8f6f4 v[54:57], v[154:157], v[62:65], v[54:57] cbsz:4 blgp:4
	v_mfma_f32_16x16x128_f8f6f4 v[58:61], v[142:145], v[66:69], v[6:9] cbsz:4 blgp:4
	v_mfma_f32_16x16x128_f8f6f4 v[58:61], v[150:153], v[70:73], v[58:61] cbsz:4 blgp:4
	v_mfma_f32_16x16x128_f8f6f4 v[62:65], v[146:149], v[66:69], v[2:5] cbsz:4 blgp:4
	v_mfma_f32_16x16x128_f8f6f4 v[62:65], v[154:157], v[70:73], v[62:65] cbsz:4 blgp:4
	v_mfma_f32_16x16x128_f8f6f4 v[66:69], v[142:145], v[74:77], v[6:9] cbsz:4 blgp:4
	v_mfma_f32_16x16x128_f8f6f4 v[66:69], v[150:153], v[78:81], v[66:69] cbsz:4 blgp:4
	v_mfma_f32_16x16x128_f8f6f4 v[70:73], v[146:149], v[74:77], v[2:5] cbsz:4 blgp:4
	v_mfma_f32_16x16x128_f8f6f4 v[70:73], v[154:157], v[78:81], v[70:73] cbsz:4 blgp:4
	v_mfma_f32_16x16x128_f8f6f4 v[74:77], v[142:145], v[86:89], v[6:9] cbsz:4 blgp:4
	v_mfma_f32_16x16x128_f8f6f4 v[74:77], v[150:153], v[90:93], v[74:77] cbsz:4 blgp:4
	v_mfma_f32_16x16x128_f8f6f4 v[78:81], v[146:149], v[86:89], v[2:5] cbsz:4 blgp:4
	v_mfma_f32_16x16x128_f8f6f4 v[78:81], v[154:157], v[90:93], v[78:81] cbsz:4 blgp:4
	s_setprio 0
	s_barrier
	s_mov_b32 m0, s54
	s_nop 0
	global_load_lds_dwordx4 v164, s[46:47]
	s_mov_b32 m0, s55
	s_nop 0
	global_load_lds_dwordx4 v168, s[46:47]
	ds_read_b128 v[114:117], v179 offset:16384
	ds_read_b128 v[122:125], v179 offset:18432
	ds_read_b128 v[130:133], v180 offset:16384
	ds_read_b128 v[134:137], v180 offset:18432
	ds_read_b128 v[158:161], v179 offset:20480
	ds_read_b128 v[182:185], v179 offset:22528
	ds_read_b128 v[186:189], v180 offset:20480
	ds_read_b128 v[190:193], v180 offset:22528
	s_mov_b32 m0, s53
	s_nop 0
	global_load_lds_dwordx4 v162, s[44:45]
	s_mov_b32 m0, s56
	s_nop 0
	global_load_lds_dwordx4 v166, s[44:45]
	s_add_u32 s46, s46, s22
	s_addc_u32 s47, s47, s23
	s_mov_b32 m0, s57
	s_nop 0
	global_load_lds_dwordx4 v164, s[46:47]
	s_mov_b32 m0, s58
	s_nop 0
	global_load_lds_dwordx4 v168, s[46:47]
	s_waitcnt vmcnt(8)
	s_waitcnt lgkmcnt(0)
	s_barrier
	s_setprio 1
	v_mfma_f32_16x16x128_f8f6f4 v[86:89], v[82:85], v[114:117], v[14:17] cbsz:4 blgp:4
	v_mfma_f32_16x16x128_f8f6f4 v[86:89], v[102:105], v[130:133], v[86:89] cbsz:4 blgp:4
	v_mfma_f32_16x16x128_f8f6f4 v[98:101], v[82:85], v[122:125], v[14:17] cbsz:4 blgp:4
	v_mfma_f32_16x16x128_f8f6f4 v[98:101], v[102:105], v[134:137], v[98:101] cbsz:4 blgp:4
	v_mfma_f32_16x16x128_f8f6f4 v[118:121], v[82:85], v[158:161], v[14:17] cbsz:4 blgp:4
	v_mfma_f32_16x16x128_f8f6f4 v[118:121], v[102:105], v[186:189], v[118:121] cbsz:4 blgp:4
	v_mfma_f32_16x16x128_f8f6f4 v[138:141], v[82:85], v[182:185], v[14:17] cbsz:4 blgp:4
	v_mfma_f32_16x16x128_f8f6f4 v[138:141], v[102:105], v[190:193], v[138:141] cbsz:4 blgp:4
	v_mfma_f32_16x16x128_f8f6f4 v[90:93], v[94:97], v[114:117], v[10:13] cbsz:4 blgp:4
	v_mfma_f32_16x16x128_f8f6f4 v[90:93], v[110:113], v[130:133], v[90:93] cbsz:4 blgp:4
	v_mfma_f32_16x16x128_f8f6f4 v[106:109], v[94:97], v[122:125], v[10:13] cbsz:4 blgp:4
	v_mfma_f32_16x16x128_f8f6f4 v[106:109], v[110:113], v[134:137], v[106:109] cbsz:4 blgp:4
	v_mfma_f32_16x16x128_f8f6f4 v[126:129], v[94:97], v[158:161], v[10:13] cbsz:4 blgp:4
	v_mfma_f32_16x16x128_f8f6f4 v[126:129], v[110:113], v[186:189], v[126:129] cbsz:4 blgp:4
	v_mfma_f32_16x16x128_f8f6f4 v[82:85], v[94:97], v[182:185], v[10:13] cbsz:4 blgp:4
	v_mfma_f32_16x16x128_f8f6f4 v[82:85], v[110:113], v[190:193], v[82:85] cbsz:4 blgp:4
	v_mfma_f32_16x16x128_f8f6f4 v[94:97], v[142:145], v[114:117], v[6:9] cbsz:4 blgp:4
	v_mfma_f32_16x16x128_f8f6f4 v[94:97], v[150:153], v[130:133], v[94:97] cbsz:4 blgp:4
	v_mfma_f32_16x16x128_f8f6f4 v[102:105], v[146:149], v[114:117], v[2:5] cbsz:4 blgp:4
	v_mfma_f32_16x16x128_f8f6f4 v[102:105], v[154:157], v[130:133], v[102:105] cbsz:4 blgp:4
	v_mfma_f32_16x16x128_f8f6f4 v[110:113], v[142:145], v[122:125], v[6:9] cbsz:4 blgp:4
	v_mfma_f32_16x16x128_f8f6f4 v[110:113], v[150:153], v[134:137], v[110:113] cbsz:4 blgp:4
	v_mfma_f32_16x16x128_f8f6f4 v[114:117], v[146:149], v[122:125], v[2:5] cbsz:4 blgp:4
	v_mfma_f32_16x16x128_f8f6f4 v[114:117], v[154:157], v[134:137], v[114:117] cbsz:4 blgp:4
	v_mfma_f32_16x16x128_f8f6f4 v[122:125], v[142:145], v[158:161], v[6:9] cbsz:4 blgp:4
	v_mfma_f32_16x16x128_f8f6f4 v[122:125], v[150:153], v[186:189], v[122:125] cbsz:4 blgp:4
	v_mfma_f32_16x16x128_f8f6f4 v[130:133], v[146:149], v[158:161], v[2:5] cbsz:4 blgp:4
	v_mfma_f32_16x16x128_f8f6f4 v[130:133], v[154:157], v[186:189], v[130:133] cbsz:4 blgp:4
	v_mfma_f32_16x16x128_f8f6f4 v[134:137], v[142:145], v[182:185], v[6:9] cbsz:4 blgp:4
	v_mfma_f32_16x16x128_f8f6f4 v[134:137], v[150:153], v[190:193], v[134:137] cbsz:4 blgp:4
	v_mfma_f32_16x16x128_f8f6f4 v[142:145], v[146:149], v[182:185], v[2:5] cbsz:4 blgp:4
	v_mfma_f32_16x16x128_f8f6f4 v[142:145], v[154:157], v[190:193], v[142:145] cbsz:4 blgp:4
	s_setprio 0
	s_barrier
	ds_read_b128 v[146:149], v169 offset:32768
	ds_read_b128 v[150:153], v169 offset:34816
	ds_read_b128 v[154:157], v178 offset:32768
	ds_read_b128 v[158:161], v178 offset:34816
	ds_read_b128 v[182:185], v179 offset:32768
	ds_read_b128 v[186:189], v179 offset:34816
	ds_read_b128 v[190:193], v180 offset:32768
	ds_read_b128 v[194:197], v180 offset:34816
	ds_read_b128 v[198:201], v179 offset:36864
	ds_read_b128 v[202:205], v179 offset:38912
	ds_read_b128 v[206:209], v180 offset:36864
	ds_read_b128 v[210:213], v180 offset:38912
	s_add_u32 s44, s44, s20
	s_addc_u32 s45, s45, s21
	s_mov_b32 m0, s59
	s_nop 0
	global_load_lds_dwordx4 v162, s[44:45]
	s_mov_b32 m0, s60
	s_nop 0
	global_load_lds_dwordx4 v166, s[44:45]
	s_waitcnt lgkmcnt(8)
	ds_read_b128 v[214:217], v169 offset:49152
	ds_read_b128 v[218:221], v169 offset:51200
	ds_read_b128 v[222:225], v178 offset:49152
	ds_read_b128 v[226:229], v178 offset:51200
	s_waitcnt vmcnt(8)
	s_waitcnt lgkmcnt(0)
	s_barrier
	s_waitcnt lgkmcnt(0)
	s_setprio 1
	v_mfma_f32_16x16x128_f8f6f4 v[18:21], v[146:149], v[182:185], v[18:21] cbsz:4 blgp:4
	v_mfma_f32_16x16x128_f8f6f4 v[18:21], v[154:157], v[190:193], v[18:21] cbsz:4 blgp:4
	v_mfma_f32_16x16x128_f8f6f4 v[26:29], v[146:149], v[186:189], v[26:29] cbsz:4 blgp:4
	v_mfma_f32_16x16x128_f8f6f4 v[26:29], v[154:157], v[194:197], v[26:29] cbsz:4 blgp:4
	v_mfma_f32_16x16x128_f8f6f4 v[34:37], v[146:149], v[198:201], v[34:37] cbsz:4 blgp:4
	v_mfma_f32_16x16x128_f8f6f4 v[34:37], v[154:157], v[206:209], v[34:37] cbsz:4 blgp:4
	v_mfma_f32_16x16x128_f8f6f4 v[42:45], v[146:149], v[202:205], v[42:45] cbsz:4 blgp:4
	v_mfma_f32_16x16x128_f8f6f4 v[42:45], v[154:157], v[210:213], v[42:45] cbsz:4 blgp:4
	v_mfma_f32_16x16x128_f8f6f4 v[22:25], v[150:153], v[182:185], v[22:25] cbsz:4 blgp:4
	v_mfma_f32_16x16x128_f8f6f4 v[22:25], v[158:161], v[190:193], v[22:25] cbsz:4 blgp:4
	v_mfma_f32_16x16x128_f8f6f4 v[30:33], v[150:153], v[186:189], v[30:33] cbsz:4 blgp:4
	v_mfma_f32_16x16x128_f8f6f4 v[30:33], v[158:161], v[194:197], v[30:33] cbsz:4 blgp:4
	v_mfma_f32_16x16x128_f8f6f4 v[38:41], v[150:153], v[198:201], v[38:41] cbsz:4 blgp:4
	v_mfma_f32_16x16x128_f8f6f4 v[38:41], v[158:161], v[206:209], v[38:41] cbsz:4 blgp:4
	v_mfma_f32_16x16x128_f8f6f4 v[46:49], v[150:153], v[202:205], v[46:49] cbsz:4 blgp:4
	v_mfma_f32_16x16x128_f8f6f4 v[46:49], v[158:161], v[210:213], v[46:49] cbsz:4 blgp:4
	v_mfma_f32_16x16x128_f8f6f4 v[50:53], v[214:217], v[182:185], v[50:53] cbsz:4 blgp:4
	v_mfma_f32_16x16x128_f8f6f4 v[50:53], v[222:225], v[190:193], v[50:53] cbsz:4 blgp:4
	v_mfma_f32_16x16x128_f8f6f4 v[58:61], v[214:217], v[186:189], v[58:61] cbsz:4 blgp:4
	v_mfma_f32_16x16x128_f8f6f4 v[58:61], v[222:225], v[194:197], v[58:61] cbsz:4 blgp:4
	v_mfma_f32_16x16x128_f8f6f4 v[66:69], v[214:217], v[198:201], v[66:69] cbsz:4 blgp:4
	v_mfma_f32_16x16x128_f8f6f4 v[66:69], v[222:225], v[206:209], v[66:69] cbsz:4 blgp:4
	v_mfma_f32_16x16x128_f8f6f4 v[74:77], v[214:217], v[202:205], v[74:77] cbsz:4 blgp:4
	v_mfma_f32_16x16x128_f8f6f4 v[74:77], v[222:225], v[210:213], v[74:77] cbsz:4 blgp:4
	v_mfma_f32_16x16x128_f8f6f4 v[54:57], v[218:221], v[182:185], v[54:57] cbsz:4 blgp:4
	v_mfma_f32_16x16x128_f8f6f4 v[54:57], v[226:229], v[190:193], v[54:57] cbsz:4 blgp:4
	v_mfma_f32_16x16x128_f8f6f4 v[62:65], v[218:221], v[186:189], v[62:65] cbsz:4 blgp:4
	v_mfma_f32_16x16x128_f8f6f4 v[62:65], v[226:229], v[194:197], v[62:65] cbsz:4 blgp:4
	v_mfma_f32_16x16x128_f8f6f4 v[70:73], v[218:221], v[198:201], v[70:73] cbsz:4 blgp:4
	v_mfma_f32_16x16x128_f8f6f4 v[70:73], v[226:229], v[206:209], v[70:73] cbsz:4 blgp:4
	v_mfma_f32_16x16x128_f8f6f4 v[78:81], v[218:221], v[202:205], v[78:81] cbsz:4 blgp:4
	v_mfma_f32_16x16x128_f8f6f4 v[78:81], v[226:229], v[210:213], v[78:81] cbsz:4 blgp:4
	s_setprio 0
	s_barrier
	s_mov_b32 m0, s62
	s_nop 0
	global_load_lds_dwordx4 v164, s[40:41]
	s_mov_b32 m0, s63
	s_nop 0
	global_load_lds_dwordx4 v168, s[40:41]
	ds_read_b128 v[182:185], v179 offset:49152
	ds_read_b128 v[186:189], v179 offset:51200
	ds_read_b128 v[190:193], v180 offset:49152
	ds_read_b128 v[194:197], v180 offset:51200
	ds_read_b128 v[198:201], v179 offset:53248
	ds_read_b128 v[202:205], v179 offset:55296
	ds_read_b128 v[206:209], v180 offset:53248
	ds_read_b128 v[210:213], v180 offset:55296
	s_mov_b32 m0, s64
	s_nop 0
	global_load_lds_dwordx4 v162, s[42:43]
	s_mov_b32 m0, s65
	s_nop 0
	global_load_lds_dwordx4 v166, s[42:43]
	s_add_u32 s40, s40, s22
	s_addc_u32 s41, s41, s23
	s_mov_b32 m0, s66
	s_nop 0
	global_load_lds_dwordx4 v164, s[40:41]
	s_mov_b32 m0, s67
	s_nop 0
	global_load_lds_dwordx4 v168, s[40:41]
	s_waitcnt vmcnt(8)
	s_waitcnt lgkmcnt(0)
	s_barrier
	s_setprio 1
	v_mfma_f32_16x16x128_f8f6f4 v[86:89], v[146:149], v[182:185], v[86:89] cbsz:4 blgp:4
	v_mfma_f32_16x16x128_f8f6f4 v[86:89], v[154:157], v[190:193], v[86:89] cbsz:4 blgp:4
	v_mfma_f32_16x16x128_f8f6f4 v[98:101], v[146:149], v[186:189], v[98:101] cbsz:4 blgp:4
	v_mfma_f32_16x16x128_f8f6f4 v[98:101], v[154:157], v[194:197], v[98:101] cbsz:4 blgp:4
	v_mfma_f32_16x16x128_f8f6f4 v[118:121], v[146:149], v[198:201], v[118:121] cbsz:4 blgp:4
	v_mfma_f32_16x16x128_f8f6f4 v[118:121], v[154:157], v[206:209], v[118:121] cbsz:4 blgp:4
	v_mfma_f32_16x16x128_f8f6f4 v[138:141], v[146:149], v[202:205], v[138:141] cbsz:4 blgp:4
	v_mfma_f32_16x16x128_f8f6f4 v[138:141], v[154:157], v[210:213], v[138:141] cbsz:4 blgp:4
	v_mfma_f32_16x16x128_f8f6f4 v[90:93], v[150:153], v[182:185], v[90:93] cbsz:4 blgp:4
	v_mfma_f32_16x16x128_f8f6f4 v[90:93], v[158:161], v[190:193], v[90:93] cbsz:4 blgp:4
	v_mfma_f32_16x16x128_f8f6f4 v[106:109], v[150:153], v[186:189], v[106:109] cbsz:4 blgp:4
	v_mfma_f32_16x16x128_f8f6f4 v[106:109], v[158:161], v[194:197], v[106:109] cbsz:4 blgp:4
	v_mfma_f32_16x16x128_f8f6f4 v[126:129], v[150:153], v[198:201], v[126:129] cbsz:4 blgp:4
	v_mfma_f32_16x16x128_f8f6f4 v[126:129], v[158:161], v[206:209], v[126:129] cbsz:4 blgp:4
	v_mfma_f32_16x16x128_f8f6f4 v[82:85], v[150:153], v[202:205], v[82:85] cbsz:4 blgp:4
	v_mfma_f32_16x16x128_f8f6f4 v[82:85], v[158:161], v[210:213], v[82:85] cbsz:4 blgp:4
	v_mfma_f32_16x16x128_f8f6f4 v[94:97], v[214:217], v[182:185], v[94:97] cbsz:4 blgp:4
	v_mfma_f32_16x16x128_f8f6f4 v[94:97], v[222:225], v[190:193], v[94:97] cbsz:4 blgp:4
	v_mfma_f32_16x16x128_f8f6f4 v[110:113], v[214:217], v[186:189], v[110:113] cbsz:4 blgp:4
	v_mfma_f32_16x16x128_f8f6f4 v[110:113], v[222:225], v[194:197], v[110:113] cbsz:4 blgp:4
	v_mfma_f32_16x16x128_f8f6f4 v[122:125], v[214:217], v[198:201], v[122:125] cbsz:4 blgp:4
	v_mfma_f32_16x16x128_f8f6f4 v[122:125], v[222:225], v[206:209], v[122:125] cbsz:4 blgp:4
	v_mfma_f32_16x16x128_f8f6f4 v[134:137], v[214:217], v[202:205], v[134:137] cbsz:4 blgp:4
	v_mfma_f32_16x16x128_f8f6f4 v[134:137], v[222:225], v[210:213], v[134:137] cbsz:4 blgp:4
	v_mfma_f32_16x16x128_f8f6f4 v[102:105], v[218:221], v[182:185], v[102:105] cbsz:4 blgp:4
	v_mfma_f32_16x16x128_f8f6f4 v[102:105], v[226:229], v[190:193], v[102:105] cbsz:4 blgp:4
	v_mfma_f32_16x16x128_f8f6f4 v[114:117], v[218:221], v[186:189], v[114:117] cbsz:4 blgp:4
	v_mfma_f32_16x16x128_f8f6f4 v[114:117], v[226:229], v[194:197], v[114:117] cbsz:4 blgp:4
	v_mfma_f32_16x16x128_f8f6f4 v[130:133], v[218:221], v[198:201], v[130:133] cbsz:4 blgp:4
	v_mfma_f32_16x16x128_f8f6f4 v[130:133], v[226:229], v[206:209], v[130:133] cbsz:4 blgp:4
	v_mfma_f32_16x16x128_f8f6f4 v[142:145], v[218:221], v[202:205], v[142:145] cbsz:4 blgp:4
	v_mfma_f32_16x16x128_f8f6f4 v[142:145], v[226:229], v[210:213], v[142:145] cbsz:4 blgp:4
	s_setprio 0
	s_andn2_b64 vcc, exec, s[28:29]
	s_barrier
	s_cbranch_vccnz .LBB6_20
	s_ashr_i32 s39, s38, 31
	s_lshl_b64 s[38:39], s[38:39], 10
	s_add_u32 s38, s14, s38
	s_addc_u32 s39, s15, s39
	s_add_u32 s31, s36, 0x200
	s_addc_u32 s46, s37, 0
	s_add_u32 s47, s34, 0x200
	s_addc_u32 s81, s35, 0
	s_add_u32 s34, s82, 0x180
	s_addc_u32 s35, s83, 0
	s_mov_b32 s82, 4
	s_cmp_eq_u32 s61, s82
	s_cselect_b64 s[36:37], -1, 0
	s_cmp_lg_u32 s61, s82
	s_cbranch_scc1 .LBB6_18

.LBB6_18:
	ds_read_b128 v[146:149], v169
	ds_read_b128 v[150:153], v169 offset:2048
	ds_read_b128 v[154:157], v178
	ds_read_b128 v[158:161], v178 offset:2048
	s_and_b64 s[36:37], s[36:37], exec
	s_cselect_b32 s42, s4, s31
	s_cselect_b32 s43, s5, s46
	s_cselect_b32 s45, s7, s81
	s_cselect_b32 s44, s6, s47
	s_add_u32 s40, s42, 0x80
	s_addc_u32 s41, s43, 0
	s_add_u32 s36, s44, 0x80
	s_addc_u32 s37, s45, 0
	ds_read_b128 v[182:185], v179
	ds_read_b128 v[186:189], v179 offset:2048
	ds_read_b128 v[190:193], v180
	ds_read_b128 v[194:197], v180 offset:2048
	ds_read_b128 v[198:201], v179 offset:4096
	ds_read_b128 v[202:205], v179 offset:6144
	ds_read_b128 v[206:209], v180 offset:4096
	ds_read_b128 v[210:213], v180 offset:6144
	s_mov_b32 m0, s68
	s_nop 0
	global_load_lds_dwordx4 v162, s[34:35]
	s_mov_b32 m0, s69
	s_nop 0
	global_load_lds_dwordx4 v166, s[34:35]
	s_waitcnt lgkmcnt(8)
	ds_read_b128 v[214:217], v169 offset:16384
	ds_read_b128 v[218:221], v169 offset:18432
	ds_read_b128 v[222:225], v178 offset:16384
	ds_read_b128 v[226:229], v178 offset:18432
	s_waitcnt vmcnt(8)
	s_waitcnt lgkmcnt(0)
	s_barrier
	s_waitcnt lgkmcnt(0)
	s_setprio 1
	v_mfma_f32_16x16x128_f8f6f4 v[18:21], v[146:149], v[182:185], v[18:21] cbsz:4 blgp:4
	v_mfma_f32_16x16x128_f8f6f4 v[18:21], v[154:157], v[190:193], v[18:21] cbsz:4 blgp:4
	v_mfma_f32_16x16x128_f8f6f4 v[26:29], v[146:149], v[186:189], v[26:29] cbsz:4 blgp:4
	v_mfma_f32_16x16x128_f8f6f4 v[26:29], v[154:157], v[194:197], v[26:29] cbsz:4 blgp:4
	v_mfma_f32_16x16x128_f8f6f4 v[34:37], v[146:149], v[198:201], v[34:37] cbsz:4 blgp:4
	v_mfma_f32_16x16x128_f8f6f4 v[34:37], v[154:157], v[206:209], v[34:37] cbsz:4 blgp:4
	v_mfma_f32_16x16x128_f8f6f4 v[42:45], v[146:149], v[202:205], v[42:45] cbsz:4 blgp:4
	v_mfma_f32_16x16x128_f8f6f4 v[42:45], v[154:157], v[210:213], v[42:45] cbsz:4 blgp:4
	v_mfma_f32_16x16x128_f8f6f4 v[22:25], v[150:153], v[182:185], v[22:25] cbsz:4 blgp:4
	v_mfma_f32_16x16x128_f8f6f4 v[22:25], v[158:161], v[190:193], v[22:25] cbsz:4 blgp:4
	v_mfma_f32_16x16x128_f8f6f4 v[30:33], v[150:153], v[186:189], v[30:33] cbsz:4 blgp:4
	v_mfma_f32_16x16x128_f8f6f4 v[30:33], v[158:161], v[194:197], v[30:33] cbsz:4 blgp:4
	v_mfma_f32_16x16x128_f8f6f4 v[38:41], v[150:153], v[198:201], v[38:41] cbsz:4 blgp:4
	v_mfma_f32_16x16x128_f8f6f4 v[38:41], v[158:161], v[206:209], v[38:41] cbsz:4 blgp:4
	v_mfma_f32_16x16x128_f8f6f4 v[46:49], v[150:153], v[202:205], v[46:49] cbsz:4 blgp:4
	v_mfma_f32_16x16x128_f8f6f4 v[46:49], v[158:161], v[210:213], v[46:49] cbsz:4 blgp:4
	v_mfma_f32_16x16x128_f8f6f4 v[50:53], v[214:217], v[182:185], v[50:53] cbsz:4 blgp:4
	v_mfma_f32_16x16x128_f8f6f4 v[50:53], v[222:225], v[190:193], v[50:53] cbsz:4 blgp:4
	v_mfma_f32_16x16x128_f8f6f4 v[58:61], v[214:217], v[186:189], v[58:61] cbsz:4 blgp:4
	v_mfma_f32_16x16x128_f8f6f4 v[58:61], v[222:225], v[194:197], v[58:61] cbsz:4 blgp:4
	v_mfma_f32_16x16x128_f8f6f4 v[66:69], v[214:217], v[198:201], v[66:69] cbsz:4 blgp:4
	v_mfma_f32_16x16x128_f8f6f4 v[66:69], v[222:225], v[206:209], v[66:69] cbsz:4 blgp:4
	v_mfma_f32_16x16x128_f8f6f4 v[74:77], v[214:217], v[202:205], v[74:77] cbsz:4 blgp:4
	v_mfma_f32_16x16x128_f8f6f4 v[74:77], v[222:225], v[210:213], v[74:77] cbsz:4 blgp:4
	v_mfma_f32_16x16x128_f8f6f4 v[54:57], v[218:221], v[182:185], v[54:57] cbsz:4 blgp:4
	v_mfma_f32_16x16x128_f8f6f4 v[54:57], v[226:229], v[190:193], v[54:57] cbsz:4 blgp:4
	v_mfma_f32_16x16x128_f8f6f4 v[62:65], v[218:221], v[186:189], v[62:65] cbsz:4 blgp:4
	v_mfma_f32_16x16x128_f8f6f4 v[62:65], v[226:229], v[194:197], v[62:65] cbsz:4 blgp:4
	v_mfma_f32_16x16x128_f8f6f4 v[70:73], v[218:221], v[198:201], v[70:73] cbsz:4 blgp:4
	v_mfma_f32_16x16x128_f8f6f4 v[70:73], v[226:229], v[206:209], v[70:73] cbsz:4 blgp:4
	v_mfma_f32_16x16x128_f8f6f4 v[78:81], v[218:221], v[202:205], v[78:81] cbsz:4 blgp:4
	v_mfma_f32_16x16x128_f8f6f4 v[78:81], v[226:229], v[210:213], v[78:81] cbsz:4 blgp:4
	s_setprio 0
	s_barrier
	s_mov_b32 m0, s54
	s_nop 0
	global_load_lds_dwordx4 v164, s[44:45]
	s_mov_b32 m0, s55
	s_nop 0
	global_load_lds_dwordx4 v168, s[44:45]
	ds_read_b128 v[182:185], v179 offset:16384
	ds_read_b128 v[186:189], v179 offset:18432
	ds_read_b128 v[190:193], v180 offset:16384
	ds_read_b128 v[194:197], v180 offset:18432
	ds_read_b128 v[198:201], v179 offset:20480
	ds_read_b128 v[202:205], v179 offset:22528
	ds_read_b128 v[206:209], v180 offset:20480
	ds_read_b128 v[210:213], v180 offset:22528
	s_mov_b32 m0, s53
	s_nop 0
	global_load_lds_dwordx4 v162, s[42:43]
	s_mov_b32 m0, s56
	s_nop 0
	global_load_lds_dwordx4 v166, s[42:43]
	s_add_u32 s44, s44, s22
	s_addc_u32 s45, s45, s23
	s_mov_b32 m0, s57
	s_nop 0
	global_load_lds_dwordx4 v164, s[44:45]
	s_mov_b32 m0, s58
	s_nop 0
	global_load_lds_dwordx4 v168, s[44:45]
	s_waitcnt vmcnt(8)
	s_waitcnt lgkmcnt(0)
	s_barrier
	s_setprio 1
	v_mfma_f32_16x16x128_f8f6f4 v[86:89], v[146:149], v[182:185], v[86:89] cbsz:4 blgp:4
	v_mfma_f32_16x16x128_f8f6f4 v[86:89], v[154:157], v[190:193], v[86:89] cbsz:4 blgp:4
	v_mfma_f32_16x16x128_f8f6f4 v[98:101], v[146:149], v[186:189], v[98:101] cbsz:4 blgp:4
	v_mfma_f32_16x16x128_f8f6f4 v[98:101], v[154:157], v[194:197], v[98:101] cbsz:4 blgp:4
	v_mfma_f32_16x16x128_f8f6f4 v[118:121], v[146:149], v[198:201], v[118:121] cbsz:4 blgp:4
	v_mfma_f32_16x16x128_f8f6f4 v[118:121], v[154:157], v[206:209], v[118:121] cbsz:4 blgp:4
	v_mfma_f32_16x16x128_f8f6f4 v[138:141], v[146:149], v[202:205], v[138:141] cbsz:4 blgp:4
	v_mfma_f32_16x16x128_f8f6f4 v[138:141], v[154:157], v[210:213], v[138:141] cbsz:4 blgp:4
	v_mfma_f32_16x16x128_f8f6f4 v[90:93], v[150:153], v[182:185], v[90:93] cbsz:4 blgp:4
	v_mfma_f32_16x16x128_f8f6f4 v[90:93], v[158:161], v[190:193], v[90:93] cbsz:4 blgp:4
	v_mfma_f32_16x16x128_f8f6f4 v[106:109], v[150:153], v[186:189], v[106:109] cbsz:4 blgp:4
	v_mfma_f32_16x16x128_f8f6f4 v[106:109], v[158:161], v[194:197], v[106:109] cbsz:4 blgp:4
	v_mfma_f32_16x16x128_f8f6f4 v[126:129], v[150:153], v[198:201], v[126:129] cbsz:4 blgp:4
	v_mfma_f32_16x16x128_f8f6f4 v[126:129], v[158:161], v[206:209], v[126:129] cbsz:4 blgp:4
	v_mfma_f32_16x16x128_f8f6f4 v[82:85], v[150:153], v[202:205], v[82:85] cbsz:4 blgp:4
	v_mfma_f32_16x16x128_f8f6f4 v[82:85], v[158:161], v[210:213], v[82:85] cbsz:4 blgp:4
	v_mfma_f32_16x16x128_f8f6f4 v[94:97], v[214:217], v[182:185], v[94:97] cbsz:4 blgp:4
	v_mfma_f32_16x16x128_f8f6f4 v[94:97], v[222:225], v[190:193], v[94:97] cbsz:4 blgp:4
	v_mfma_f32_16x16x128_f8f6f4 v[110:113], v[214:217], v[186:189], v[110:113] cbsz:4 blgp:4
	v_mfma_f32_16x16x128_f8f6f4 v[110:113], v[222:225], v[194:197], v[110:113] cbsz:4 blgp:4
	v_mfma_f32_16x16x128_f8f6f4 v[122:125], v[214:217], v[198:201], v[122:125] cbsz:4 blgp:4
	v_mfma_f32_16x16x128_f8f6f4 v[122:125], v[222:225], v[206:209], v[122:125] cbsz:4 blgp:4
	v_mfma_f32_16x16x128_f8f6f4 v[134:137], v[214:217], v[202:205], v[134:137] cbsz:4 blgp:4
	v_mfma_f32_16x16x128_f8f6f4 v[134:137], v[222:225], v[210:213], v[134:137] cbsz:4 blgp:4
	v_mfma_f32_16x16x128_f8f6f4 v[102:105], v[218:221], v[182:185], v[102:105] cbsz:4 blgp:4
	v_mfma_f32_16x16x128_f8f6f4 v[102:105], v[226:229], v[190:193], v[102:105] cbsz:4 blgp:4
	v_mfma_f32_16x16x128_f8f6f4 v[114:117], v[218:221], v[186:189], v[114:117] cbsz:4 blgp:4
	v_mfma_f32_16x16x128_f8f6f4 v[114:117], v[226:229], v[194:197], v[114:117] cbsz:4 blgp:4
	v_mfma_f32_16x16x128_f8f6f4 v[130:133], v[218:221], v[198:201], v[130:133] cbsz:4 blgp:4
	v_mfma_f32_16x16x128_f8f6f4 v[130:133], v[226:229], v[206:209], v[130:133] cbsz:4 blgp:4
	v_mfma_f32_16x16x128_f8f6f4 v[142:145], v[218:221], v[202:205], v[142:145] cbsz:4 blgp:4
	v_mfma_f32_16x16x128_f8f6f4 v[142:145], v[226:229], v[210:213], v[142:145] cbsz:4 blgp:4
	s_setprio 0
	s_barrier
	ds_read_b128 v[146:149], v169 offset:32768
	ds_read_b128 v[150:153], v169 offset:34816
	ds_read_b128 v[154:157], v178 offset:32768
	ds_read_b128 v[158:161], v178 offset:34816
	ds_read_b128 v[182:185], v179 offset:32768
	ds_read_b128 v[186:189], v179 offset:34816
	ds_read_b128 v[190:193], v180 offset:32768
	ds_read_b128 v[194:197], v180 offset:34816
	ds_read_b128 v[198:201], v179 offset:36864
	ds_read_b128 v[202:205], v179 offset:38912
	ds_read_b128 v[206:209], v180 offset:36864
	ds_read_b128 v[210:213], v180 offset:38912
	s_add_u32 s42, s42, s20
	s_addc_u32 s43, s43, s21
	s_mov_b32 m0, s59
	s_nop 0
	global_load_lds_dwordx4 v162, s[42:43]
	s_mov_b32 m0, s60
	s_nop 0
	global_load_lds_dwordx4 v166, s[42:43]
	s_waitcnt lgkmcnt(8)
	ds_read_b128 v[214:217], v169 offset:49152
	ds_read_b128 v[218:221], v169 offset:51200
	ds_read_b128 v[222:225], v178 offset:49152
	ds_read_b128 v[226:229], v178 offset:51200
	s_waitcnt vmcnt(8)
	s_waitcnt lgkmcnt(0)
	s_barrier
	s_waitcnt lgkmcnt(0)
	s_setprio 1
	v_mfma_f32_16x16x128_f8f6f4 v[18:21], v[146:149], v[182:185], v[18:21] cbsz:4 blgp:4
	v_mfma_f32_16x16x128_f8f6f4 v[18:21], v[154:157], v[190:193], v[18:21] cbsz:4 blgp:4
	v_mfma_f32_16x16x128_f8f6f4 v[26:29], v[146:149], v[186:189], v[26:29] cbsz:4 blgp:4
	v_mfma_f32_16x16x128_f8f6f4 v[26:29], v[154:157], v[194:197], v[26:29] cbsz:4 blgp:4
	v_mfma_f32_16x16x128_f8f6f4 v[34:37], v[146:149], v[198:201], v[34:37] cbsz:4 blgp:4
	v_mfma_f32_16x16x128_f8f6f4 v[34:37], v[154:157], v[206:209], v[34:37] cbsz:4 blgp:4
	v_mfma_f32_16x16x128_f8f6f4 v[42:45], v[146:149], v[202:205], v[42:45] cbsz:4 blgp:4
	v_mfma_f32_16x16x128_f8f6f4 v[42:45], v[154:157], v[210:213], v[42:45] cbsz:4 blgp:4
	v_mfma_f32_16x16x128_f8f6f4 v[22:25], v[150:153], v[182:185], v[22:25] cbsz:4 blgp:4
	v_mfma_f32_16x16x128_f8f6f4 v[22:25], v[158:161], v[190:193], v[22:25] cbsz:4 blgp:4
	v_mfma_f32_16x16x128_f8f6f4 v[30:33], v[150:153], v[186:189], v[30:33] cbsz:4 blgp:4
	v_mfma_f32_16x16x128_f8f6f4 v[30:33], v[158:161], v[194:197], v[30:33] cbsz:4 blgp:4
	v_mfma_f32_16x16x128_f8f6f4 v[38:41], v[150:153], v[198:201], v[38:41] cbsz:4 blgp:4
	v_mfma_f32_16x16x128_f8f6f4 v[38:41], v[158:161], v[206:209], v[38:41] cbsz:4 blgp:4
	v_mfma_f32_16x16x128_f8f6f4 v[46:49], v[150:153], v[202:205], v[46:49] cbsz:4 blgp:4
	v_mfma_f32_16x16x128_f8f6f4 v[46:49], v[158:161], v[210:213], v[46:49] cbsz:4 blgp:4
	v_mfma_f32_16x16x128_f8f6f4 v[50:53], v[214:217], v[182:185], v[50:53] cbsz:4 blgp:4
	v_mfma_f32_16x16x128_f8f6f4 v[50:53], v[222:225], v[190:193], v[50:53] cbsz:4 blgp:4
	v_mfma_f32_16x16x128_f8f6f4 v[58:61], v[214:217], v[186:189], v[58:61] cbsz:4 blgp:4
	v_mfma_f32_16x16x128_f8f6f4 v[58:61], v[222:225], v[194:197], v[58:61] cbsz:4 blgp:4
	v_mfma_f32_16x16x128_f8f6f4 v[66:69], v[214:217], v[198:201], v[66:69] cbsz:4 blgp:4
	v_mfma_f32_16x16x128_f8f6f4 v[66:69], v[222:225], v[206:209], v[66:69] cbsz:4 blgp:4
	v_mfma_f32_16x16x128_f8f6f4 v[74:77], v[214:217], v[202:205], v[74:77] cbsz:4 blgp:4
	v_mfma_f32_16x16x128_f8f6f4 v[74:77], v[222:225], v[210:213], v[74:77] cbsz:4 blgp:4
	v_mfma_f32_16x16x128_f8f6f4 v[54:57], v[218:221], v[182:185], v[54:57] cbsz:4 blgp:4
	v_mfma_f32_16x16x128_f8f6f4 v[54:57], v[226:229], v[190:193], v[54:57] cbsz:4 blgp:4
	v_mfma_f32_16x16x128_f8f6f4 v[62:65], v[218:221], v[186:189], v[62:65] cbsz:4 blgp:4
	v_mfma_f32_16x16x128_f8f6f4 v[62:65], v[226:229], v[194:197], v[62:65] cbsz:4 blgp:4
	v_mfma_f32_16x16x128_f8f6f4 v[70:73], v[218:221], v[198:201], v[70:73] cbsz:4 blgp:4
	v_mfma_f32_16x16x128_f8f6f4 v[70:73], v[226:229], v[206:209], v[70:73] cbsz:4 blgp:4
	v_mfma_f32_16x16x128_f8f6f4 v[78:81], v[218:221], v[202:205], v[78:81] cbsz:4 blgp:4
	v_mfma_f32_16x16x128_f8f6f4 v[78:81], v[226:229], v[210:213], v[78:81] cbsz:4 blgp:4
	s_setprio 0
	s_barrier
	s_mov_b32 m0, s62
	s_nop 0
	global_load_lds_dwordx4 v164, s[36:37]
	s_mov_b32 m0, s63
	s_nop 0
	global_load_lds_dwordx4 v168, s[36:37]
	ds_read_b128 v[182:185], v179 offset:49152
	ds_read_b128 v[186:189], v179 offset:51200
	ds_read_b128 v[190:193], v180 offset:49152
	ds_read_b128 v[194:197], v180 offset:51200
	ds_read_b128 v[198:201], v179 offset:53248
	ds_read_b128 v[202:205], v179 offset:55296
	ds_read_b128 v[206:209], v180 offset:53248
	ds_read_b128 v[210:213], v180 offset:55296
	s_mov_b32 m0, s64
	s_nop 0
	global_load_lds_dwordx4 v162, s[40:41]
	s_mov_b32 m0, s65
	s_nop 0
	global_load_lds_dwordx4 v166, s[40:41]
	s_add_u32 s36, s36, s22
	s_addc_u32 s37, s37, s23
	s_mov_b32 m0, s66
	s_nop 0
	global_load_lds_dwordx4 v164, s[36:37]
	s_mov_b32 m0, s67
	s_nop 0
	global_load_lds_dwordx4 v168, s[36:37]
	s_waitcnt vmcnt(8)
	s_waitcnt lgkmcnt(0)
	s_barrier
	s_setprio 1
	v_mfma_f32_16x16x128_f8f6f4 v[86:89], v[146:149], v[182:185], v[86:89] cbsz:4 blgp:4
	v_mfma_f32_16x16x128_f8f6f4 v[86:89], v[154:157], v[190:193], v[86:89] cbsz:4 blgp:4
	v_mfma_f32_16x16x128_f8f6f4 v[98:101], v[146:149], v[186:189], v[98:101] cbsz:4 blgp:4
	v_mfma_f32_16x16x128_f8f6f4 v[98:101], v[154:157], v[194:197], v[98:101] cbsz:4 blgp:4
	v_mfma_f32_16x16x128_f8f6f4 v[118:121], v[146:149], v[198:201], v[118:121] cbsz:4 blgp:4
	v_mfma_f32_16x16x128_f8f6f4 v[118:121], v[154:157], v[206:209], v[118:121] cbsz:4 blgp:4
	v_mfma_f32_16x16x128_f8f6f4 v[138:141], v[146:149], v[202:205], v[138:141] cbsz:4 blgp:4
	v_mfma_f32_16x16x128_f8f6f4 v[138:141], v[154:157], v[210:213], v[138:141] cbsz:4 blgp:4
	v_mfma_f32_16x16x128_f8f6f4 v[90:93], v[150:153], v[182:185], v[90:93] cbsz:4 blgp:4
	v_mfma_f32_16x16x128_f8f6f4 v[90:93], v[158:161], v[190:193], v[90:93] cbsz:4 blgp:4
	v_mfma_f32_16x16x128_f8f6f4 v[106:109], v[150:153], v[186:189], v[106:109] cbsz:4 blgp:4
	v_mfma_f32_16x16x128_f8f6f4 v[106:109], v[158:161], v[194:197], v[106:109] cbsz:4 blgp:4
	v_mfma_f32_16x16x128_f8f6f4 v[126:129], v[150:153], v[198:201], v[126:129] cbsz:4 blgp:4
	v_mfma_f32_16x16x128_f8f6f4 v[126:129], v[158:161], v[206:209], v[126:129] cbsz:4 blgp:4
	v_mfma_f32_16x16x128_f8f6f4 v[82:85], v[150:153], v[202:205], v[82:85] cbsz:4 blgp:4
	v_mfma_f32_16x16x128_f8f6f4 v[82:85], v[158:161], v[210:213], v[82:85] cbsz:4 blgp:4
	v_mfma_f32_16x16x128_f8f6f4 v[94:97], v[214:217], v[182:185], v[94:97] cbsz:4 blgp:4
	v_mfma_f32_16x16x128_f8f6f4 v[94:97], v[222:225], v[190:193], v[94:97] cbsz:4 blgp:4
	v_mfma_f32_16x16x128_f8f6f4 v[110:113], v[214:217], v[186:189], v[110:113] cbsz:4 blgp:4
	v_mfma_f32_16x16x128_f8f6f4 v[110:113], v[222:225], v[194:197], v[110:113] cbsz:4 blgp:4
	v_mfma_f32_16x16x128_f8f6f4 v[122:125], v[214:217], v[198:201], v[122:125] cbsz:4 blgp:4
	v_mfma_f32_16x16x128_f8f6f4 v[122:125], v[222:225], v[206:209], v[122:125] cbsz:4 blgp:4
	v_mfma_f32_16x16x128_f8f6f4 v[134:137], v[214:217], v[202:205], v[134:137] cbsz:4 blgp:4
	v_mfma_f32_16x16x128_f8f6f4 v[134:137], v[222:225], v[210:213], v[134:137] cbsz:4 blgp:4
	v_mfma_f32_16x16x128_f8f6f4 v[102:105], v[218:221], v[182:185], v[102:105] cbsz:4 blgp:4
	v_mfma_f32_16x16x128_f8f6f4 v[102:105], v[226:229], v[190:193], v[102:105] cbsz:4 blgp:4
	v_mfma_f32_16x16x128_f8f6f4 v[114:117], v[218:221], v[186:189], v[114:117] cbsz:4 blgp:4
	v_mfma_f32_16x16x128_f8f6f4 v[114:117], v[226:229], v[194:197], v[114:117] cbsz:4 blgp:4
	v_mfma_f32_16x16x128_f8f6f4 v[130:133], v[218:221], v[198:201], v[130:133] cbsz:4 blgp:4
	v_mfma_f32_16x16x128_f8f6f4 v[130:133], v[226:229], v[206:209], v[130:133] cbsz:4 blgp:4
	v_mfma_f32_16x16x128_f8f6f4 v[142:145], v[218:221], v[202:205], v[142:145] cbsz:4 blgp:4
	v_mfma_f32_16x16x128_f8f6f4 v[142:145], v[226:229], v[210:213], v[142:145] cbsz:4 blgp:4
	s_setprio 0
	s_add_i32 s36, s82, 2
	s_add_u32 s31, s31, 0x100
	s_addc_u32 s46, s46, 0
	s_add_u32 s47, s47, 0x100
	s_addc_u32 s81, s81, 0
	s_add_u32 s34, s34, 0x100
	s_addc_u32 s35, s35, 0
	s_cmp_ge_i32 s82, s61
	s_barrier
	s_cbranch_scc1 .LBB6_20
	s_mov_b32 s82, s36
	s_cmp_eq_u32 s61, s82
	s_cselect_b64 s[36:37], -1, 0
	s_cmp_lg_u32 s61, s82
	s_cbranch_scc0 .LBB6_17
	s_branch .LBB6_18
